# bonus-scalar producer: 8-value reduce-scatter butterfly instead of eight full 64-lane reductions; merge GEMM epilogue touches the second row half's gate vectors early; router bias loaded once per phas
# speedup vs baseline: 1.0293x; 1.0008x over previous
; __device__ __forceinline__ void p4a_chunk(Frame& F0, const In& I) {
;     ...
;     for (int unit = F.vcu; unit < BATCH * RH * (SEQ / 64); unit += F.G, ++uit) {
;         const int bh = unit >> 7, ck = unit & 127, b = bh >> 4, h = bh & 15;
;         const size_t tok0 = (size_t)b * SEQ + (size_t)ck * 64 + 8 * w;
;         const int hc = h * 64 + lane;
;         float lwv[8], ic[8], rr[8], kk[8], vv[8];
; #pragma unroll
;         for (int i = 0; i < 8; ++i) { const size_t tok = tok0 + i; lwv[i] = LW[tok * RW + hc]; ic[i] = bf2f(ICL[tok * RW + hc]);
;             rr[i] = bf2f(RKV[tok * (3 * RW) + hc]); kk[i] = bf2f(RKV[tok * (3 * RW) + RW + hc]); vv[i] = bf2f(RKV[tok * (3 * RW) + 2 * RW + hc]); }
;         const float kkp = I.k_k[hc], kap = I.k_a[hc];
.LBB0_1083:
	s_ashr_i32 s14, s13, 11
	s_ashr_i32 s15, s14, 31
	s_lshl_b64 s[14:15], s[14:15], 13
	s_and_b32 s16, s33, 0x1fc0
	s_add_u32 s16, s16, s22
	s_addc_u32 s17, 0, s23
	s_add_u32 s14, s16, s14
	s_addc_u32 s15, s17, s15
	s_lshr_b32 s16, s13, 1
	s_and_b32 s16, s16, 0x3c0
	s_waitcnt vmcnt(12)
	v_readlane_b32 s56, v254, 27
	v_readlane_b32 s57, v254, 28
	v_or_b32_e32 v88, s16, v1
	s_lshl_b64 s[16:17], s[14:15], 10
	v_or_b32_e32 v82, s16, v88
	s_mulk_i32 s15, 0x1800
	s_mul_hi_u32 s16, s14, 0x1800
	v_mov_b32_e32 v83, s17
	s_add_i32 s16, s16, s15
	s_mulk_i32 s14, 0x1800
	v_readlane_b32 s20, v254, 54
	v_lshl_add_u64 v[80:81], v[82:83], 2, s[0:1]
	v_readlane_b32 s21, v254, 55
	s_add_u32 s14, s20, s14
	global_load_dword v89, v[80:81], off
	v_lshl_add_u64 v[80:81], v[82:83], 1, s[88:89]
	s_addc_u32 s15, s21, s16
	v_lshlrev_b32_e32 v68, 1, v88
	global_load_ushort v84, v[80:81], off
	v_lshl_add_u64 v[80:81], s[14:15], 0, v[68:69]
	global_load_ushort v90, v68, s[14:15]
	global_load_ushort v85, v68, s[14:15] offset:2048
	s_movk_i32 s14, 0x1000
	v_add_co_u32_e32 v86, vcc, s14, v80
	s_mov_b64 s[14:15], 0x400
	v_lshl_add_u64 v[92:93], v[82:83], 0, s[14:15]
	v_addc_co_u32_e32 v87, vcc, 0, v81, vcc
	v_lshl_add_u64 v[94:95], v[92:93], 2, s[0:1]
	v_lshl_add_u64 v[92:93], v[92:93], 1, s[88:89]
	s_movk_i32 s14, 0x2000
	global_load_ushort v168, v[86:87], off
	v_readlane_b32 s48, v254, 21
	global_load_dword v94, v[94:95], off
	v_lshlrev_b32_e32 v68, 2, v88
	global_load_ushort v95, v[92:93], off
	v_lshl_add_u64 v[92:93], v[80:81], 0, s[78:79]
	global_load_ushort v96, v[86:87], off offset:2048
	global_load_ushort v91, v[92:93], off offset:2048
	v_add_co_u32_e32 v86, vcc, s14, v80
	s_mov_b64 s[14:15], 0x800
	s_nop 0
	v_addc_co_u32_e32 v87, vcc, 0, v81, vcc
	global_load_ushort v169, v[86:87], off offset:2048
	v_lshl_add_u64 v[86:87], v[82:83], 0, s[14:15]
	v_lshl_add_u64 v[92:93], v[86:87], 2, s[0:1]
	v_lshl_add_u64 v[86:87], v[86:87], 1, s[88:89]
	s_mov_b64 s[14:15], 0x3000
	global_load_dword v104, v[92:93], off
	global_load_ushort v97, v[86:87], off
	v_lshl_add_u64 v[86:87], v[80:81], 0, s[14:15]
	s_movk_i32 s14, 0x4000
	v_add_co_u32_e32 v92, vcc, s14, v80
	s_mov_b64 s[14:15], 0xc00
	s_nop 0
	v_addc_co_u32_e32 v93, vcc, 0, v81, vcc
	global_load_ushort v99, v[92:93], off offset:-4096
	global_load_ushort v98, v[86:87], off offset:2048
	global_load_ushort v170, v[92:93], off
	v_lshl_add_u64 v[86:87], v[82:83], 0, s[14:15]
	v_lshl_add_u64 v[100:101], v[86:87], 2, s[0:1]
	v_lshl_add_u64 v[86:87], v[86:87], 1, s[88:89]
	s_mov_b64 s[14:15], 0x4800
	global_load_dword v105, v[100:101], off
	global_load_ushort v102, v[86:87], off
	v_lshl_add_u64 v[86:87], v[80:81], 0, s[14:15]
	s_movk_i32 s14, 0x5000
	global_load_ushort v106, v[92:93], off offset:2048
	global_load_ushort v103, v[86:87], off offset:2048
	v_add_co_u32_e32 v86, vcc, s14, v80
	s_mov_b64 s[14:15], 0x1000
	s_nop 0
	v_addc_co_u32_e32 v87, vcc, 0, v81, vcc
	global_load_ushort v171, v[86:87], off offset:2048
	v_lshl_add_u64 v[86:87], v[82:83], 0, s[14:15]
	v_lshl_add_u64 v[92:93], v[86:87], 2, s[0:1]
	v_lshl_add_u64 v[86:87], v[86:87], 1, s[88:89]
	s_mov_b64 s[14:15], 0x6000
	global_load_dword v108, v[92:93], off
	global_load_ushort v110, v[86:87], off
	v_lshl_add_u64 v[86:87], v[80:81], 0, s[14:15]
	s_movk_i32 s14, 0x7000
	v_add_co_u32_e32 v92, vcc, s14, v80
	s_mov_b64 s[14:15], 0x1400
	s_nop 0
	v_addc_co_u32_e32 v93, vcc, 0, v81, vcc
	global_load_ushort v112, v[92:93], off offset:-4096
	global_load_ushort v107, v[86:87], off offset:2048
	global_load_ushort v172, v[92:93], off
	v_lshl_add_u64 v[86:87], v[82:83], 0, s[14:15]
	v_lshl_add_u64 v[100:101], v[86:87], 2, s[0:1]
	v_lshl_add_u64 v[86:87], v[86:87], 1, s[88:89]
	s_mov_b64 s[14:15], 0x7800
	global_load_dword v100, v[100:101], off
	v_readlane_b32 s50, v254, 23
	global_load_ushort v113, v[86:87], off
	v_lshl_add_u64 v[86:87], v[80:81], 0, s[14:15]
	s_mov_b32 s14, 0x8000
	global_load_ushort v114, v[92:93], off offset:2048
	global_load_ushort v111, v[86:87], off offset:2048
	v_add_co_u32_e32 v86, vcc, s14, v80
	s_mov_b64 s[14:15], 0x9000
	s_nop 0
	v_addc_co_u32_e32 v87, vcc, 0, v81, vcc
	global_load_ushort v173, v[86:87], off offset:2048
	v_lshl_add_u64 v[86:87], v[82:83], 0, s[78:79]
	v_lshl_add_u64 v[92:93], v[86:87], 2, s[0:1]
	v_lshl_add_u64 v[86:87], v[86:87], 1, s[88:89]
	global_load_dword v101, v[92:93], off
	global_load_ushort v176, v[86:87], off
	v_lshl_add_u64 v[86:87], v[80:81], 0, s[14:15]
	s_mov_b32 s14, 0xa000
	v_add_co_u32_e32 v92, vcc, s14, v80
	s_mov_b64 s[14:15], 0x1c00
	s_nop 0
	v_addc_co_u32_e32 v93, vcc, 0, v81, vcc
	v_lshl_add_u64 v[82:83], v[82:83], 0, s[14:15]
	global_load_ushort v177, v[92:93], off offset:-4096
	global_load_ushort v115, v[86:87], off offset:2048
	global_load_ushort v174, v[92:93], off
	v_lshl_add_u64 v[86:87], v[82:83], 2, s[0:1]
	global_load_dword v86, v[86:87], off
	v_lshl_add_u64 v[82:83], v[82:83], 1, s[88:89]
	s_mov_b64 s[14:15], 0xa800
	global_load_ushort v186, v[82:83], off
	v_lshl_add_u64 v[82:83], v[80:81], 0, s[14:15]
	s_mov_b32 s14, 0xb000
	v_add_co_u32_e32 v80, vcc, s14, v80
	v_readlane_b32 s51, v254, 24
	s_nop 0
	v_addc_co_u32_e32 v81, vcc, 0, v81, vcc
	global_load_ushort v188, v[92:93], off offset:2048
	global_load_ushort v182, v[82:83], off offset:2048
	global_load_ushort v175, v[80:81], off offset:2048
	v_readlane_b32 s52, v254, 25
	v_readlane_b32 s53, v254, 26
	global_load_dword v88, v68, s[50:51]
	s_nop 3
	global_load_dword v230, v68, s[56:57]
	global_load_dword v68, v68, s[52:53]
	s_waitcnt vmcnt(0)
; __device__ __forceinline__ float quadsum(float x) { x += dpp_f(x, 0); x += dpp_f(x, 1); return x; }
; __device__ __forceinline__ void p4a_chunk(Frame& F0, const In& I) {
;     ...
;             const float kkv = kk[i] * kkp; const float n2 = wave_sum(kkv * kkv); const float kkn = kkv * __builtin_amdgcn_rsqf(fmaxf(n2, 1e-24f));
;             const float a = -kkn, bb = kkn * ic[i], kp = kk[i] * (1.0f + (ic[i] - 1.0f) * kap);
; __device__ __forceinline__ void p5_post(Frame& F0, const In& I) {
;     ...
;         for (int e = 0; e < 16; ++e) { s += y[e]; const float kp = kk[e] * (1.0f + (ic[e] - 1.0f) * p_ka[e]); bs += rr[e] * kp * p_rk[e]; }
;         s = quadsum(s); bs = quadsum(bs);
	v_lshlrev_b32_e32 v231, 16, v84
	v_lshlrev_b32_e32 v232, 16, v85
	v_lshlrev_b32_e32 v233, 16, v90
	v_add_f32_e32 v231, -1.0, v231
	v_fma_f32 v231, v231, v68, 1.0
	v_mul_f32_e32 v232, v232, v231
	v_mul_f32_e32 v233, v233, v232
	v_mul_f32_e32 v234, v233, v230
	v_lshlrev_b32_e32 v231, 16, v95
	v_lshlrev_b32_e32 v232, 16, v91
	v_lshlrev_b32_e32 v233, 16, v96
	v_add_f32_e32 v231, -1.0, v231
	v_fma_f32 v231, v231, v68, 1.0
	v_mul_f32_e32 v232, v232, v231
	v_mul_f32_e32 v233, v233, v232
	v_mul_f32_e32 v235, v233, v230
	v_lshlrev_b32_e32 v231, 16, v97
	v_lshlrev_b32_e32 v232, 16, v98
	v_lshlrev_b32_e32 v233, 16, v99
	v_add_f32_e32 v231, -1.0, v231
	v_fma_f32 v231, v231, v68, 1.0
	v_mul_f32_e32 v232, v232, v231
	v_mul_f32_e32 v233, v233, v232
	v_mul_f32_e32 v236, v233, v230
	v_lshlrev_b32_e32 v231, 16, v102
	v_lshlrev_b32_e32 v232, 16, v103
	v_lshlrev_b32_e32 v233, 16, v106
	v_add_f32_e32 v231, -1.0, v231
	v_fma_f32 v231, v231, v68, 1.0
	v_mul_f32_e32 v232, v232, v231
	v_mul_f32_e32 v233, v233, v232
	v_mul_f32_e32 v237, v233, v230
	v_lshlrev_b32_e32 v231, 16, v110
	v_lshlrev_b32_e32 v232, 16, v107
	v_lshlrev_b32_e32 v233, 16, v112
	v_add_f32_e32 v231, -1.0, v231
	v_fma_f32 v231, v231, v68, 1.0
	v_mul_f32_e32 v232, v232, v231
	v_mul_f32_e32 v233, v233, v232
	v_mul_f32_e32 v238, v233, v230
	v_lshlrev_b32_e32 v231, 16, v113
	v_lshlrev_b32_e32 v232, 16, v111
	v_lshlrev_b32_e32 v233, 16, v114
	v_add_f32_e32 v231, -1.0, v231
	v_fma_f32 v231, v231, v68, 1.0
	v_mul_f32_e32 v232, v232, v231
	v_mul_f32_e32 v233, v233, v232
	v_mul_f32_e32 v239, v233, v230
	v_lshlrev_b32_e32 v231, 16, v176
	v_lshlrev_b32_e32 v232, 16, v115
	v_lshlrev_b32_e32 v233, 16, v177
	v_add_f32_e32 v231, -1.0, v231
	v_fma_f32 v231, v231, v68, 1.0
	v_mul_f32_e32 v232, v232, v231
	v_mul_f32_e32 v233, v233, v232
	v_mul_f32_e32 v240, v233, v230
	v_lshlrev_b32_e32 v231, 16, v186
	v_lshlrev_b32_e32 v232, 16, v182
	v_lshlrev_b32_e32 v233, 16, v188
	v_add_f32_e32 v231, -1.0, v231
	v_fma_f32 v231, v231, v68, 1.0
	v_mul_f32_e32 v232, v232, v231
	v_mul_f32_e32 v233, v233, v232
	v_mul_f32_e32 v241, v233, v230
	s_mov_b32 s58, 0xaaaaaaaa
	s_mov_b32 s59, 0xaaaaaaaa
	s_mov_b32 s60, 0xcccccccc
	s_mov_b32 s61, 0xcccccccc
	s_mov_b32 s54, 0xff00ff00
	s_mov_b32 s55, 0xff00ff00
	v_cndmask_b32_e64 v231, v235, v234, s[58:59]
	v_cndmask_b32_e64 v232, v237, v236, s[58:59]
	v_cndmask_b32_e64 v233, v239, v238, s[58:59]
	v_cndmask_b32_e64 v242, v241, v240, s[58:59]
	v_cndmask_b32_e64 v234, v234, v235, s[58:59]
	v_cndmask_b32_e64 v236, v236, v237, s[58:59]
	v_cndmask_b32_e64 v238, v238, v239, s[58:59]
	v_cndmask_b32_e64 v240, v240, v241, s[58:59]
	v_add_f32_dpp v234, v231, v234 quad_perm:[1,0,3,2] row_mask:0xf bank_mask:0xf
	v_add_f32_dpp v236, v232, v236 quad_perm:[1,0,3,2] row_mask:0xf bank_mask:0xf
	v_add_f32_dpp v238, v233, v238 quad_perm:[1,0,3,2] row_mask:0xf bank_mask:0xf
	v_add_f32_dpp v240, v242, v240 quad_perm:[1,0,3,2] row_mask:0xf bank_mask:0xf
	s_nop 1
	v_cndmask_b32_e64 v231, v236, v234, s[60:61]
	v_cndmask_b32_e64 v232, v240, v238, s[60:61]
	v_cndmask_b32_e64 v234, v234, v236, s[60:61]
	v_cndmask_b32_e64 v238, v238, v240, s[60:61]
	s_nop 0
	v_add_f32_dpp v234, v231, v234 quad_perm:[2,3,0,1] row_mask:0xf bank_mask:0xf
	v_add_f32_dpp v238, v232, v238 quad_perm:[2,3,0,1] row_mask:0xf bank_mask:0xf
	s_nop 1
	v_cndmask_b32_e64 v231, v238, v234, s[54:55]
	v_cndmask_b32_e64 v234, v234, v238, s[54:55]
	s_nop 1
	v_add_f32_dpp v234, v231, v234 row_ror:8 row_mask:0xf bank_mask:0xf
	s_nop 1
	v_add_f32_dpp v234, v234, v234 row_shr:4 row_mask:0xf bank_mask:0xf bound_ctrl:1
	s_nop 1
	v_mov_b32_e32 v231, v234
	s_nop 1
	v_permlane32_swap_b32_e32 v231, v234
	s_nop 1
	v_add_f32_e32 v234, v231, v234
	v_mov_b32_e32 v231, v234
	s_nop 1
	v_permlane16_swap_b32_e32 v231, v234
	s_nop 1
	v_add_f32_e32 v234, v231, v234
	s_ashr_i32 s48, s13, 11
	s_lshl_b32 s48, s48, 13
	s_lshl_b32 s49, s13, 6
	s_and_b32 s49, s49, 0x1fc0
	s_add_i32 s49, s49, s22
	s_add_i32 s48, s48, s49
	s_lshl_b32 s48, s48, 6
	s_lshr_b32 s49, s13, 5
	s_and_b32 s49, s49, 0x3c
	s_add_i32 s48, s48, s49
	v_and_b32_e32 v232, 3, v1
	v_lshrrev_b32_e32 v233, 1, v1
	v_and_b32_e32 v233, 4, v233
	v_or_b32_e32 v232, v232, v233
	v_lshl_add_u32 v243, v232, 6, s48
	s_add_u32 s50, s96, 0x1c00000
	s_addc_u32 s51, s97, 0
	s_mov_b64 s[62:63], exec
	s_mov_b64 exec, 0xf0f0
	global_store_dword v243, v234, s[50:51]
	s_mov_b64 exec, s[62:63]
	s_cmp_gt_i32 s85, 0xffff
	s_cbranch_scc1 .Lxs_down
	s_lshr_b32 s49, s85, 11
	s_lshl_b32 s49, s49, 25
	s_bfe_u32 s54, s85, 0x50006
	s_lshl_b32 s54, s54, 20
	s_add_i32 s49, s49, s54
	s_and_b32 s54, s85, 63
	s_lshl_b32 s54, s54, 8
	s_add_i32 s49, s49, s54
	s_mov_b32 s55, 0x10000
	s_movk_i32 s56, 0x4000
	v_readlane_b32 s60, v255, 54
	v_readlane_b32 s61, v255, 55
	s_branch .Lxs_go

;     __device__ __forceinline__ bool operator()(f32x4 (&acc)[2][2][4][2], const Unit& u, int wr, int wc, int fr, int fq) const {
;     ...
;         const u32x4* gf = (const u32x4*)PROJ + ((size_t)(u.pm * 16 + u.pn * 2) * 2 * 8 + (u.aux == 0 ? 0 : 8) + (wr * 4 + wc)) * 512 + (fq * 16 + fr);
; #pragma unroll
;         for (int ai = 0; ai < 2; ++ai) {
;             u32x4 gv[4][2];
; #pragma unroll
;             for (int m = 0; m < 4; ++m)
; #pragma unroll
;                 for (int bj = 0; bj < 2; ++bj) gv[m][bj] = gf[(size_t)bj * (2 * 8 * 512) + (ai * 4 + m) * 64];
; #pragma unroll
;             for (int m = 0; m < 4; ++m) { const int row = row0 + ai * HALF + m * 16;
; #pragma unroll
;                 for (int bj = 0; bj < 2; ++bj) { const u32x4 g = gv[m][bj];
;                     const f32x4 g0 = (f32x4){bflo(g.x), bfhi(g.x), bflo(g.y), bfhi(g.y)}, g1 = (f32x4){bflo(g.z), bfhi(g.z), bflo(g.w), bfhi(g.w)};
;                     if (u.aux == 0) { acc[ai][bj][m][0] = acc[ai][bj][m][0] * g0; acc[ai][bj][m][1] = acc[ai][bj][m][1] * g1; }
.LBB0_1292:
	v_mov_b32_e32 v5, v0
	s_lshl_b32 s54, s8, 8
	v_readfirstlane_b32 s6, v5
	s_bfe_u32 s53, s6, 0x20006
	s_ashr_i32 s27, s6, 8
	s_lshl_b32 s6, s9, 8
	s_lshl_b32 s7, s53, 5
	s_or_b32 s6, s7, s6
	v_lshrrev_b32_e32 v2, 1, v5
	v_and_or_b32 v4, v2, 24, s6
	s_lshl_b32 s6, s8, 4
	s_lshl_b32 s7, s9, 1
	s_add_i32 s6, s6, s7
	s_ashr_i32 s7, s6, 31
	s_cmp_lg_u32 s26, 0
	s_cselect_b64 s[24:25], -1, 0
	s_cmp_eq_u32 s26, 0
	s_cselect_b32 s8, 0, 8
	s_lshl_b32 s9, s27, 2
	s_or_b32 s9, s9, s53
	s_ashr_i32 s26, s9, 31
	s_add_u32 s8, s8, s9
	s_addc_u32 s9, 0, s26
	s_lshl_b64 s[6:7], s[6:7], 17
	s_lshl_b64 s[8:9], s[8:9], 13
	s_add_u32 s6, s56, s6
	s_addc_u32 s7, s57, s7
	s_add_u32 s6, s6, s8
	v_and_b32_e32 v2, 63, v5
	s_addc_u32 s7, s7, s9
	v_lshlrev_b32_e32 v2, 4, v2
	v_lshl_add_u64 v[176:177], s[6:7], 0, v[2:3]
	v_add_co_u32_e32 v150, vcc, s46, v176
	v_add_u32_e32 v114, 0x1000, v2
	v_add_u32_e32 v115, s46, v114
	global_load_dwordx4 v[94:97], v114, s[6:7]
	global_load_dwordx4 v[94:97], v115, s[6:7]
	global_load_dwordx4 v[94:97], v114, s[6:7] offset:1024
	global_load_dwordx4 v[94:97], v115, s[6:7] offset:1024
	global_load_dwordx4 v[94:97], v114, s[6:7] offset:2048
	global_load_dwordx4 v[94:97], v115, s[6:7] offset:2048
	global_load_dwordx4 v[94:97], v114, s[6:7] offset:3072
	global_load_dwordx4 v[94:97], v115, s[6:7] offset:3072
	global_load_dwordx4 v[94:97], v2, s[6:7]
	s_nop 0
	v_addc_co_u32_e32 v151, vcc, 0, v177, vcc
	global_load_dwordx4 v[162:165], v[150:151], off
	global_load_dwordx4 v[114:117], v2, s[6:7] offset:1024
	global_load_dwordx4 v[158:161], v[150:151], off offset:1024
	global_load_dwordx4 v[130:133], v2, s[6:7] offset:2048
	global_load_dwordx4 v[154:157], v[150:151], off offset:2048
	global_load_dwordx4 v[142:145], v2, s[6:7] offset:3072
	s_nop 0
	global_load_dwordx4 v[150:153], v[150:151], off offset:3072
	v_and_or_b32 v5, v5, 15, s54
	v_lshl_add_u32 v174, s27, 6, v5
	v_ashrrev_i32_e32 v175, 31, v174
	v_lshlrev_b64 v[166:167], 11, v[174:175]
	v_ashrrev_i32_e32 v5, 31, v4
	s_mov_b64 s[6:7], -1
	s_and_b64 vcc, exec, s[24:25]
	s_waitcnt vmcnt(7)
	v_lshlrev_b32_e32 v170, 16, v94
	v_and_b32_e32 v171, 0xffff0000, v94
	v_lshlrev_b32_e32 v94, 16, v95
	v_and_b32_e32 v95, 0xffff0000, v95
	v_lshlrev_b32_e32 v172, 16, v96
	v_and_b32_e32 v173, 0xffff0000, v96
	v_lshlrev_b32_e32 v168, 16, v97
	v_and_b32_e32 v169, 0xffff0000, v97
	v_pk_mul_f32 v[96:97], v[108:109], v[94:95]
	v_pk_mul_f32 v[94:95], v[106:107], v[170:171]
	v_lshl_add_u64 v[170:171], s[10:11], 0, v[166:167]
	v_pk_mul_f32 v[166:167], v[66:67], v[172:173]
	v_lshl_add_u64 v[178:179], v[170:171], 0, v[4:5]
	s_cbranch_vccz .LBB0_1294
	v_pk_mul_f32 v[172:173], v[94:95], s[14:15] op_sel_hi:[1,0]
	v_pk_mul_f32 v[184:185], v[166:167], s[14:15] op_sel_hi:[1,0]
	v_mov_b32_e32 v186, v3
	v_mov_b32_e32 v187, v3
	v_cvt_pk_fp8_f32 v186, v172, v173
	v_cvt_pk_fp8_f32 v187, v184, v185
	v_pk_mul_f32 v[172:173], v[68:69], v[168:169]
	v_pk_mul_f32 v[170:171], v[96:97], s[14:15] op_sel_hi:[1,0]
	v_pk_mul_f32 v[172:173], v[172:173], s[14:15] op_sel_hi:[1,0]
	v_cvt_pk_fp8_f32 v186, v170, v171 op_sel:[0,0,1]
	v_cvt_pk_fp8_f32 v187, v172, v173 op_sel:[0,0,1]
	s_mov_b64 s[6:7], 0
	global_store_dwordx2 v[178:179], v[186:187], off

; #define GAS __attribute__((address_space(1)))
; #define LAS __attribute__((address_space(3)))
; template <bool SKIP_MIX>
; __device__ __forceinline__ void p8_ln_router(Frame& F0, const In& I) {
;     ...
;     LAS float* hs = (LAS float*)(F.lds + P8_HS); LAS float* part = (LAS float*)(F.lds + P8_PART); LAS float* lg = (LAS float*)(F.lds + P8_LOG); LAS int* hist = (LAS int*)(F.lds + P8_HIST);
;     const int lane = F.lane, w = F.wave;
;     if (F.tid < 32) hist[F.tid] = 0;
;     const int kq = lane >> 4, col = lane & 15;
;     float ln_w[32], ln_b[32];
; #pragma unroll
;     for (int j = 0; j < 8; ++j) { const f32x4 a = *(const GAS f32x4*)(I.ln1_w + 4 * lane + 256 * j), b = *(const GAS f32x4*)(I.ln1_b + 4 * lane + 256 * j);
; #pragma unroll
;         for (int e = 0; e < 4; ++e) { ln_w[4 * j + e] = a[e]; ln_b[4 * j + e] = b[e]; } }
;     __syncthreads();
;     if (F.vcu & 1) { __builtin_amdgcn_s_sleep(127); __builtin_amdgcn_s_sleep(127); }
;     const float* zsrc = I.x; const bf16* mixb = (const bf16*)(F.ws + WS_Z);
;     for (int g = F.vcu; g < T / 16; g += F.G) {
.LBB0_1511:
	v_readlane_b32 s0, v254, 62
	v_readlane_b32 s1, v254, 63
	s_andn2_b64 vcc, exec, s[0:1]
	s_cbranch_vccnz .LBB0_1518
	s_ashr_i32 s12, s4, 6
	v_lshrrev_b32_e32 v70, 2, v74
	v_and_b32_e32 v67, 15, v74
	s_lshl_b32 s0, s12, 10
	v_and_b32_e32 v70, 12, v70
	v_mul_u32_u24_e32 v69, 0x2010, v67
	s_add_i32 s0, s0, 0
	v_lshlrev_b32_e32 v71, 2, v70
	s_lshl_b32 s8, s12, 1
	v_add3_u32 v152, s0, v69, v71
	s_add_i32 s0, 0, 0x20100
	s_add_i32 s1, 0, 0x24100
	s_add_u32 s6, s96, 0x200000
	s_addc_u32 s7, s97, 0
	v_readlane_b32 s36, v254, 37
	v_lshlrev_b32_e32 v69, 2, v67
	v_and_b32_e32 v67, 0x3fffffe0, v74
	v_lshlrev_b32_e32 v71, 2, v74
	s_add_u32 s10, s96, 0x300000
	v_readlane_b32 s37, v254, 38
	v_readlane_b32 s38, v254, 39
	v_readlane_b32 s39, v254, 40
	v_readlane_b32 s40, v254, 41
	v_readlane_b32 s41, v254, 42
	v_readlane_b32 s42, v254, 43
	v_readlane_b32 s43, v254, 44
	v_readlane_b32 s44, v254, 45
	v_readlane_b32 s45, v254, 46
	v_readlane_b32 s46, v254, 47
	v_readlane_b32 s47, v254, 48
	v_readlane_b32 s48, v254, 49
	v_readlane_b32 s49, v254, 50
	v_readlane_b32 s50, v254, 51
	v_readlane_b32 s51, v254, 52
	v_lshlrev_b32_e32 v67, 2, v67
	v_and_b32_e32 v76, 0x7c, v71
	v_add_u32_e32 v154, s1, v71
	s_addc_u32 s11, s97, 0
	s_lshl_b32 s1, s12, 11
	v_mov_b32_e32 v77, 0
	s_mov_b64 s[14:15], s[42:43]
	s_mov_b64 s[16:17], s[44:45]
	v_readlane_b32 s36, v254, 5
	v_add3_u32 v153, s0, v67, v76
	s_add_i32 s1, s1, s0
	v_lshl_add_u64 v[78:79], s[16:17], 0, v[76:77]
	v_mov_b32_e32 v67, v77
	v_readlane_b32 s37, v254, 6
	v_lshlrev_b32_e32 v76, 3, v68
	v_add_u32_e32 v75, 0, v66
	v_add_u32_e32 v73, s1, v69
	v_lshl_add_u64 v[80:81], s[36:37], 0, v[66:67]
	v_lshl_add_u64 v[82:83], s[56:57], 0, v[76:77]
	v_lshl_add_u64 v[66:67], s[96:97], 0, v[76:77]
	s_mov_b64 s[0:1], 0xc0000000
	v_lshlrev_b32_e32 v76, 2, v68
	v_lshl_add_u64 v[84:85], v[66:67], 0, s[0:1]
	v_lshl_add_u64 v[66:67], s[96:97], 0, v[76:77]
	s_mov_b64 s[0:1], 0xd0000000
	v_lshl_add_u64 v[86:87], v[66:67], 0, s[0:1]
	v_lshl_or_b32 v66, s12, 8, v70
	v_ashrrev_i32_e32 v67, 31, v66
	v_lshlrev_b64 v[66:67], 7, v[66:67]
	v_lshlrev_b32_e32 v71, 7, v74
	v_or_b32_e32 v66, v66, v69
	s_or_b32 s13, s8, 1
	v_lshlrev_b32_e32 v72, 7, v70
	v_lshl_add_u64 v[88:89], s[14:15], 0, v[66:67]
	v_add_u32_e32 v66, 0, v71
	v_cmp_gt_i32_e64 s[4:5], 16, v74
	s_mul_i32 s9, s12, 0x4020
	s_mul_i32 s18, s13, 0x2010
	s_movk_i32 s19, 0x1000
	s_mov_b32 s12, 0x3f9837f0
	v_mov_b32_e32 v76, 0x3727c5ac
	s_mov_b32 s20, 0xf800000
	v_mov_b32_e32 v155, 0x260
	v_add_u32_e32 v156, v73, v72
	v_add_u32_e32 v157, 0x24100, v66
	v_mov_b32_e32 v158, 1
	s_add_i32 s21, 0, 0x24900
	v_mov_b32_e32 v159, 0xff7fc99e
	s_mov_b32 s22, s70
	v_readlane_b32 s38, v254, 7
	v_readlane_b32 s39, v254, 8
	v_readlane_b32 s40, v254, 9
	v_readlane_b32 s41, v254, 10
	v_readlane_b32 s42, v254, 11
	v_readlane_b32 s43, v254, 12
	v_readlane_b32 s44, v254, 13
	v_readlane_b32 s45, v254, 14
	v_readlane_b32 s46, v254, 15
	v_readlane_b32 s47, v254, 16
	v_readlane_b32 s48, v254, 17
	v_readlane_b32 s49, v254, 18
	v_readlane_b32 s50, v254, 19
	v_readlane_b32 s51, v254, 20
	s_waitcnt vmcnt(0)
	global_load_dword v253, v[78:79], off
	s_mov_b64 s[0:1], 0x1000
	v_mov_b32_e32 v108, v88
	v_mov_b32_e32 v109, v89
	v_lshl_add_u64 v[108:109], v[108:109], 0, s[0:1]
	v_lshl_add_u64 v[108:109], v[108:109], 0, s[0:1]
	v_lshl_add_u64 v[108:109], v[108:109], 0, s[0:1]
	v_lshl_add_u64 v[108:109], v[108:109], 0, s[0:1]
	global_load_dword v200, v[108:109], off offset:2240
	global_load_dword v201, v[108:109], off offset:2304
	global_load_dword v202, v[108:109], off offset:2368
	global_load_dword v203, v[108:109], off offset:2432
	global_load_dword v204, v[108:109], off offset:2496
	v_lshl_add_u64 v[108:109], v[108:109], 0, s[0:1]
	global_load_dword v205, v[108:109], off offset:0
	global_load_dword v206, v[108:109], off offset:64
	global_load_dword v207, v[108:109], off offset:128
	global_load_dword v208, v[108:109], off offset:192
	global_load_dword v209, v[108:109], off offset:256
	global_load_dword v210, v[108:109], off offset:320
	global_load_dword v211, v[108:109], off offset:384
	global_load_dword v212, v[108:109], off offset:448
	global_load_dword v213, v[108:109], off offset:2048
	global_load_dword v214, v[108:109], off offset:2112
	global_load_dword v215, v[108:109], off offset:2176
	global_load_dword v216, v[108:109], off offset:2240
	global_load_dword v217, v[108:109], off offset:2304
	global_load_dword v218, v[108:109], off offset:2368
	global_load_dword v219, v[108:109], off offset:2432
	global_load_dword v220, v[108:109], off offset:2496
	v_lshl_add_u64 v[108:109], v[108:109], 0, s[0:1]
	global_load_dword v221, v[108:109], off offset:0
	global_load_dword v222, v[108:109], off offset:64
	global_load_dword v223, v[108:109], off offset:128
	global_load_dword v224, v[108:109], off offset:192
	global_load_dword v225, v[108:109], off offset:256
	global_load_dword v226, v[108:109], off offset:320
	global_load_dword v227, v[108:109], off offset:384
	global_load_dword v228, v[108:109], off offset:448
	global_load_dword v229, v[108:109], off offset:2048
	global_load_dword v230, v[108:109], off offset:2112
	global_load_dword v231, v[108:109], off offset:2176
	global_load_dword v232, v[108:109], off offset:2240
	global_load_dword v233, v[108:109], off offset:2304
	global_load_dword v234, v[108:109], off offset:2368
	global_load_dword v235, v[108:109], off offset:2432
	global_load_dword v236, v[108:109], off offset:2496
	v_lshl_add_u64 v[108:109], v[108:109], 0, s[0:1]
	global_load_dword v237, v[108:109], off offset:0
	global_load_dword v238, v[108:109], off offset:64
	global_load_dword v239, v[108:109], off offset:128
	global_load_dword v240, v[108:109], off offset:192
	global_load_dword v241, v[108:109], off offset:256
	global_load_dword v242, v[108:109], off offset:320
	global_load_dword v243, v[108:109], off offset:384
	global_load_dword v244, v[108:109], off offset:448
	global_load_dword v245, v[108:109], off offset:2048
	global_load_dword v246, v[108:109], off offset:2112
	global_load_dword v247, v[108:109], off offset:2176
	global_load_dword v248, v[108:109], off offset:2240
	global_load_dword v249, v[108:109], off offset:2304
	global_load_dword v250, v[108:109], off offset:2368
	global_load_dword v251, v[108:109], off offset:2432
	global_load_dword v252, v[108:109], off offset:2496
	s_waitcnt vmcnt(0)
	s_branch .LBB0_1514

; #define LAS __attribute__((address_space(3)))
; template <bool SKIP_MIX>
; __device__ __forceinline__ void p8_ln_router(Frame& F0, const In& I) {
;     ...
;         const LAS float* ap = hs + col * P8_PITCH + 256 * w + 4 * kq;
;         const float* bp = I.w_router + (size_t)(256 * w + 4 * kq) * NE + col;
; #pragma unroll 4
;         for (int kk = 0; kk < 16; ++kk) {
;             const f32x4 a = *(const LAS f32x4*)(ap + 16 * kk);
; #pragma unroll
;             for (int e = 0; e < 4; ++e) {
;                 const float b0 = bp[(size_t)(16 * kk + e) * NE], b1 = bp[(size_t)(16 * kk + e) * NE + 16];
;                 c0 = __builtin_amdgcn_mfma_f32_16x16x4f32(a[e], b0, c0, 0, 0, 0);
;                 c1 = __builtin_amdgcn_mfma_f32_16x16x4f32(a[e], b1, c1, 0, 0, 0);
;             }
;         }
.LBB0_1515:
	s_waitcnt vmcnt(16)
	s_mov_b64 s[0:1], 0x1000
	v_mov_b32_e32 v108, v88
	v_mov_b32_e32 v109, v89
	global_load_dword v117, v[108:109], off offset:0
	global_load_dword v118, v[108:109], off offset:64
	global_load_dword v119, v[108:109], off offset:128
	global_load_dword v120, v[108:109], off offset:192
	global_load_dword v121, v[108:109], off offset:256
	global_load_dword v122, v[108:109], off offset:320
	global_load_dword v123, v[108:109], off offset:384
	global_load_dword v124, v[108:109], off offset:448
	global_load_dword v125, v[108:109], off offset:2048
	global_load_dword v126, v[108:109], off offset:2112
	global_load_dword v127, v[108:109], off offset:2176
	global_load_dword v128, v[108:109], off offset:2240
	global_load_dword v129, v[108:109], off offset:2304
	global_load_dword v130, v[108:109], off offset:2368
	global_load_dword v131, v[108:109], off offset:2432
	global_load_dword v132, v[108:109], off offset:2496
	v_lshl_add_u64 v[108:109], v[108:109], 0, s[0:1]
	global_load_dword v133, v[108:109], off offset:0
	global_load_dword v134, v[108:109], off offset:64
	global_load_dword v135, v[108:109], off offset:128
	global_load_dword v136, v[108:109], off offset:192
	global_load_dword v137, v[108:109], off offset:256
	global_load_dword v138, v[108:109], off offset:320
	global_load_dword v139, v[108:109], off offset:384
	global_load_dword v140, v[108:109], off offset:448
	global_load_dword v141, v[108:109], off offset:2048
	global_load_dword v142, v[108:109], off offset:2112
	global_load_dword v143, v[108:109], off offset:2176
	global_load_dword v144, v[108:109], off offset:2240
	global_load_dword v145, v[108:109], off offset:2304
	global_load_dword v146, v[108:109], off offset:2368
	global_load_dword v147, v[108:109], off offset:2432
	global_load_dword v148, v[108:109], off offset:2496
	v_lshl_add_u64 v[108:109], v[108:109], 0, s[0:1]
	global_load_dword v149, v[108:109], off offset:0
	global_load_dword v150, v[108:109], off offset:64
	global_load_dword v151, v[108:109], off offset:128
	global_load_dword v160, v[108:109], off offset:192
	global_load_dword v161, v[108:109], off offset:256
	global_load_dword v162, v[108:109], off offset:320
	global_load_dword v163, v[108:109], off offset:384
	global_load_dword v164, v[108:109], off offset:448
	global_load_dword v165, v[108:109], off offset:2048
	global_load_dword v166, v[108:109], off offset:2112
	global_load_dword v167, v[108:109], off offset:2176
	global_load_dword v168, v[108:109], off offset:2240
	ds_read_b128 v[92:95], v90
	ds_read_b128 v[96:99], v90 offset:64
	ds_read_b128 v[100:103], v90 offset:128
	ds_read_b128 v[104:107], v90 offset:192
	s_waitcnt lgkmcnt(3)
	global_load_dword v169, v[108:109], off offset:2304
	s_waitcnt vmcnt(43)
	v_mfma_f32_16x16x4_f32 v[66:69], v92, v117, v[66:69]
	v_mfma_f32_16x16x4_f32 v[70:73], v92, v118, v[70:73]
	global_load_dword v170, v[108:109], off offset:2368
	s_waitcnt vmcnt(42)
	v_mfma_f32_16x16x4_f32 v[66:69], v93, v119, v[66:69]
	v_mfma_f32_16x16x4_f32 v[70:73], v93, v120, v[70:73]
	global_load_dword v171, v[108:109], off offset:2432
	s_waitcnt vmcnt(41)
	v_mfma_f32_16x16x4_f32 v[66:69], v94, v121, v[66:69]
	v_mfma_f32_16x16x4_f32 v[70:73], v94, v122, v[70:73]
	global_load_dword v172, v[108:109], off offset:2496
	s_waitcnt vmcnt(40)
	v_mfma_f32_16x16x4_f32 v[66:69], v95, v123, v[66:69]
	v_mfma_f32_16x16x4_f32 v[70:73], v95, v124, v[70:73]
	s_waitcnt lgkmcnt(2)
	v_lshl_add_u64 v[108:109], v[108:109], 0, s[0:1]
	global_load_dword v173, v[108:109], off offset:0
	s_waitcnt vmcnt(39)
	v_mfma_f32_16x16x4_f32 v[66:69], v96, v125, v[66:69]
	v_mfma_f32_16x16x4_f32 v[70:73], v96, v126, v[70:73]
	global_load_dword v174, v[108:109], off offset:64
	s_waitcnt vmcnt(38)
	v_mfma_f32_16x16x4_f32 v[66:69], v97, v127, v[66:69]
	v_mfma_f32_16x16x4_f32 v[70:73], v97, v128, v[70:73]
	global_load_dword v175, v[108:109], off offset:128
	s_waitcnt vmcnt(37)
	v_mfma_f32_16x16x4_f32 v[66:69], v98, v129, v[66:69]
	v_mfma_f32_16x16x4_f32 v[70:73], v98, v130, v[70:73]
	global_load_dword v176, v[108:109], off offset:192
	s_waitcnt vmcnt(36)
	v_mfma_f32_16x16x4_f32 v[66:69], v99, v131, v[66:69]
	v_mfma_f32_16x16x4_f32 v[70:73], v99, v132, v[70:73]
	s_waitcnt lgkmcnt(1)
	global_load_dword v177, v[108:109], off offset:256
	s_waitcnt vmcnt(35)
	v_mfma_f32_16x16x4_f32 v[66:69], v100, v133, v[66:69]
	v_mfma_f32_16x16x4_f32 v[70:73], v100, v134, v[70:73]
	global_load_dword v178, v[108:109], off offset:320
	s_waitcnt vmcnt(34)
	v_mfma_f32_16x16x4_f32 v[66:69], v101, v135, v[66:69]
	v_mfma_f32_16x16x4_f32 v[70:73], v101, v136, v[70:73]
	global_load_dword v179, v[108:109], off offset:384
	s_waitcnt vmcnt(33)
	v_mfma_f32_16x16x4_f32 v[66:69], v102, v137, v[66:69]
	v_mfma_f32_16x16x4_f32 v[70:73], v102, v138, v[70:73]
	global_load_dword v180, v[108:109], off offset:448
	s_waitcnt vmcnt(32)
	v_mfma_f32_16x16x4_f32 v[66:69], v103, v139, v[66:69]
	v_mfma_f32_16x16x4_f32 v[70:73], v103, v140, v[70:73]
	s_waitcnt lgkmcnt(0)
	global_load_dword v181, v[108:109], off offset:2048
	s_waitcnt vmcnt(31)
	v_mfma_f32_16x16x4_f32 v[66:69], v104, v141, v[66:69]
	v_mfma_f32_16x16x4_f32 v[70:73], v104, v142, v[70:73]
	global_load_dword v182, v[108:109], off offset:2112
	s_waitcnt vmcnt(30)
	v_mfma_f32_16x16x4_f32 v[66:69], v105, v143, v[66:69]
	v_mfma_f32_16x16x4_f32 v[70:73], v105, v144, v[70:73]
	global_load_dword v183, v[108:109], off offset:2176
	s_waitcnt vmcnt(29)
	v_mfma_f32_16x16x4_f32 v[66:69], v106, v145, v[66:69]
	v_mfma_f32_16x16x4_f32 v[70:73], v106, v146, v[70:73]
	global_load_dword v184, v[108:109], off offset:2240
	s_waitcnt vmcnt(28)
; #define LAS __attribute__((address_space(3)))
; template <bool SKIP_MIX>
; __device__ __forceinline__ void p8_ln_router(Frame& F0, const In& I) {
;     ...
;         const LAS float* ap = hs + col * P8_PITCH + 256 * w + 4 * kq;
;         const float* bp = I.w_router + (size_t)(256 * w + 4 * kq) * NE + col;
; #pragma unroll 4
;         for (int kk = 0; kk < 16; ++kk) {
;             const f32x4 a = *(const LAS f32x4*)(ap + 16 * kk);
; #pragma unroll
;             for (int e = 0; e < 4; ++e) {
;                 const float b0 = bp[(size_t)(16 * kk + e) * NE], b1 = bp[(size_t)(16 * kk + e) * NE + 16];
;                 c0 = __builtin_amdgcn_mfma_f32_16x16x4f32(a[e], b0, c0, 0, 0, 0);
;                 c1 = __builtin_amdgcn_mfma_f32_16x16x4f32(a[e], b1, c1, 0, 0, 0);
;             }
;         }
	v_mfma_f32_16x16x4_f32 v[66:69], v107, v147, v[66:69]
	v_mfma_f32_16x16x4_f32 v[70:73], v107, v148, v[70:73]
	ds_read_b128 v[92:95], v90 offset:256
	ds_read_b128 v[96:99], v90 offset:320
	ds_read_b128 v[100:103], v90 offset:384
	ds_read_b128 v[104:107], v90 offset:448
	s_waitcnt lgkmcnt(3)
	global_load_dword v185, v[108:109], off offset:2304
	s_waitcnt vmcnt(27)
	v_mfma_f32_16x16x4_f32 v[66:69], v92, v149, v[66:69]
	v_mfma_f32_16x16x4_f32 v[70:73], v92, v150, v[70:73]
	global_load_dword v186, v[108:109], off offset:2368
	s_waitcnt vmcnt(26)
	v_mfma_f32_16x16x4_f32 v[66:69], v93, v151, v[66:69]
	v_mfma_f32_16x16x4_f32 v[70:73], v93, v160, v[70:73]
	global_load_dword v187, v[108:109], off offset:2432
	s_waitcnt vmcnt(25)
	v_mfma_f32_16x16x4_f32 v[66:69], v94, v161, v[66:69]
	v_mfma_f32_16x16x4_f32 v[70:73], v94, v162, v[70:73]
	global_load_dword v188, v[108:109], off offset:2496
	s_waitcnt vmcnt(24)
	v_mfma_f32_16x16x4_f32 v[66:69], v95, v163, v[66:69]
	v_mfma_f32_16x16x4_f32 v[70:73], v95, v164, v[70:73]
	s_waitcnt lgkmcnt(2)
	v_lshl_add_u64 v[108:109], v[108:109], 0, s[0:1]
	global_load_dword v189, v[108:109], off offset:0
	s_waitcnt vmcnt(23)
	v_mfma_f32_16x16x4_f32 v[66:69], v96, v165, v[66:69]
	v_mfma_f32_16x16x4_f32 v[70:73], v96, v166, v[70:73]
	global_load_dword v190, v[108:109], off offset:64
	s_waitcnt vmcnt(22)
	v_mfma_f32_16x16x4_f32 v[66:69], v97, v167, v[66:69]
	v_mfma_f32_16x16x4_f32 v[70:73], v97, v168, v[70:73]
	global_load_dword v191, v[108:109], off offset:128
	s_waitcnt vmcnt(21)
	v_mfma_f32_16x16x4_f32 v[66:69], v98, v169, v[66:69]
	v_mfma_f32_16x16x4_f32 v[70:73], v98, v170, v[70:73]
	global_load_dword v192, v[108:109], off offset:192
	s_waitcnt vmcnt(20)
	v_mfma_f32_16x16x4_f32 v[66:69], v99, v171, v[66:69]
	v_mfma_f32_16x16x4_f32 v[70:73], v99, v172, v[70:73]
	s_waitcnt lgkmcnt(1)
	global_load_dword v193, v[108:109], off offset:256
	s_waitcnt vmcnt(19)
	v_mfma_f32_16x16x4_f32 v[66:69], v100, v173, v[66:69]
	v_mfma_f32_16x16x4_f32 v[70:73], v100, v174, v[70:73]
	global_load_dword v194, v[108:109], off offset:320
	s_waitcnt vmcnt(18)
	v_mfma_f32_16x16x4_f32 v[66:69], v101, v175, v[66:69]
	v_mfma_f32_16x16x4_f32 v[70:73], v101, v176, v[70:73]
	global_load_dword v195, v[108:109], off offset:384
	s_waitcnt vmcnt(17)
	v_mfma_f32_16x16x4_f32 v[66:69], v102, v177, v[66:69]
	v_mfma_f32_16x16x4_f32 v[70:73], v102, v178, v[70:73]
	global_load_dword v196, v[108:109], off offset:448
	s_waitcnt vmcnt(16)
	v_mfma_f32_16x16x4_f32 v[66:69], v103, v179, v[66:69]
	v_mfma_f32_16x16x4_f32 v[70:73], v103, v180, v[70:73]
	s_waitcnt lgkmcnt(0)
	global_load_dword v197, v[108:109], off offset:2048
	s_waitcnt vmcnt(15)
	v_mfma_f32_16x16x4_f32 v[66:69], v104, v181, v[66:69]
	v_mfma_f32_16x16x4_f32 v[70:73], v104, v182, v[70:73]
	global_load_dword v198, v[108:109], off offset:2112
	s_waitcnt vmcnt(14)
	v_mfma_f32_16x16x4_f32 v[66:69], v105, v183, v[66:69]
	v_mfma_f32_16x16x4_f32 v[70:73], v105, v184, v[70:73]
	global_load_dword v199, v[108:109], off offset:2176
	s_waitcnt vmcnt(13)
	v_mfma_f32_16x16x4_f32 v[66:69], v106, v185, v[66:69]
	v_mfma_f32_16x16x4_f32 v[70:73], v106, v186, v[70:73]
	s_waitcnt vmcnt(11)
	v_mfma_f32_16x16x4_f32 v[66:69], v107, v187, v[66:69]
	v_mfma_f32_16x16x4_f32 v[70:73], v107, v188, v[70:73]
	ds_read_b128 v[92:95], v90 offset:512
	ds_read_b128 v[96:99], v90 offset:576
	ds_read_b128 v[100:103], v90 offset:640
	ds_read_b128 v[104:107], v90 offset:704
	s_waitcnt lgkmcnt(3)
	s_waitcnt vmcnt(9)
	v_mfma_f32_16x16x4_f32 v[66:69], v92, v189, v[66:69]
	v_mfma_f32_16x16x4_f32 v[70:73], v92, v190, v[70:73]
	s_waitcnt vmcnt(7)
	v_mfma_f32_16x16x4_f32 v[66:69], v93, v191, v[66:69]
	v_mfma_f32_16x16x4_f32 v[70:73], v93, v192, v[70:73]
	s_waitcnt vmcnt(5)
	v_mfma_f32_16x16x4_f32 v[66:69], v94, v193, v[66:69]
	v_mfma_f32_16x16x4_f32 v[70:73], v94, v194, v[70:73]
	s_waitcnt vmcnt(3)
	v_mfma_f32_16x16x4_f32 v[66:69], v95, v195, v[66:69]
	v_mfma_f32_16x16x4_f32 v[70:73], v95, v196, v[70:73]
	s_waitcnt lgkmcnt(2)
	s_waitcnt vmcnt(1)
	v_mfma_f32_16x16x4_f32 v[66:69], v96, v197, v[66:69]
	v_mfma_f32_16x16x4_f32 v[70:73], v96, v198, v[70:73]
	s_waitcnt vmcnt(0)
	v_mfma_f32_16x16x4_f32 v[66:69], v97, v199, v[66:69]
	v_mfma_f32_16x16x4_f32 v[70:73], v97, v200, v[70:73]
	v_mfma_f32_16x16x4_f32 v[66:69], v98, v201, v[66:69]
	v_mfma_f32_16x16x4_f32 v[70:73], v98, v202, v[70:73]
	v_mfma_f32_16x16x4_f32 v[66:69], v99, v203, v[66:69]
	v_mfma_f32_16x16x4_f32 v[70:73], v99, v204, v[70:73]
	s_waitcnt lgkmcnt(1)
	v_mfma_f32_16x16x4_f32 v[66:69], v100, v205, v[66:69]
	v_mfma_f32_16x16x4_f32 v[70:73], v100, v206, v[70:73]
	v_mfma_f32_16x16x4_f32 v[66:69], v101, v207, v[66:69]
	v_mfma_f32_16x16x4_f32 v[70:73], v101, v208, v[70:73]
	v_mfma_f32_16x16x4_f32 v[66:69], v102, v209, v[66:69]
	v_mfma_f32_16x16x4_f32 v[70:73], v102, v210, v[70:73]
	v_mfma_f32_16x16x4_f32 v[66:69], v103, v211, v[66:69]
	v_mfma_f32_16x16x4_f32 v[70:73], v103, v212, v[70:73]
	s_waitcnt lgkmcnt(0)
	v_mfma_f32_16x16x4_f32 v[66:69], v104, v213, v[66:69]
	v_mfma_f32_16x16x4_f32 v[70:73], v104, v214, v[70:73]
	v_mfma_f32_16x16x4_f32 v[66:69], v105, v215, v[66:69]
	v_mfma_f32_16x16x4_f32 v[70:73], v105, v216, v[70:73]
	v_mfma_f32_16x16x4_f32 v[66:69], v106, v217, v[66:69]
	v_mfma_f32_16x16x4_f32 v[70:73], v106, v218, v[70:73]
	v_mfma_f32_16x16x4_f32 v[66:69], v107, v219, v[66:69]
	v_mfma_f32_16x16x4_f32 v[70:73], v107, v220, v[70:73]
	ds_read_b128 v[92:95], v90 offset:768
	ds_read_b128 v[96:99], v90 offset:832
	ds_read_b128 v[100:103], v90 offset:896
	ds_read_b128 v[104:107], v90 offset:960
	s_waitcnt lgkmcnt(3)
; #define LAS __attribute__((address_space(3)))
; template <bool SKIP_MIX>
; __device__ __forceinline__ void p8_ln_router(Frame& F0, const In& I) {
;     ...
;         for (int kk = 0; kk < 16; ++kk) {
;             const f32x4 a = *(const LAS f32x4*)(ap + 16 * kk);
; #pragma unroll
;             for (int e = 0; e < 4; ++e) {
;                 const float b0 = bp[(size_t)(16 * kk + e) * NE], b1 = bp[(size_t)(16 * kk + e) * NE + 16];
;                 c0 = __builtin_amdgcn_mfma_f32_16x16x4f32(a[e], b0, c0, 0, 0, 0);
;                 c1 = __builtin_amdgcn_mfma_f32_16x16x4f32(a[e], b1, c1, 0, 0, 0);
;             }
;         }
; #pragma unroll
;         for (int i = 0; i < 4; ++i) { part[(w * 16 + 4 * kq + i) * 32 + col] = c0[i]; part[(w * 16 + 4 * kq + i) * 32 + 16 + col] = c1[i]; }
;         __syncthreads();
;         { const int tl = F.tid >> 5, e = F.tid & 31; float s = I.b_router[e];
; #pragma unroll
;             for (int ww = 0; ww < 8; ++ww) s += part[(ww * 16 + tl) * 32 + e];
;             lg[tl * 32 + e] = s; }
;         __syncthreads();
;         if (F.tid < 16) {
;             const int tl = F.tid; float lv[32];
; #pragma unroll
;             for (int e = 0; e < 32; ++e) lv[e] = lg[tl * 32 + e];
;             int ti[4]; float tv[4];
; #pragma unroll
;             for (int k = 0; k < 4; ++k) { float best = -3.4e38f; int bi = 0;
; #pragma unroll
;                 for (int e = 0; e < 32; ++e) { const bool tk = lv[e] > best; best = tk ? lv[e] : best; bi = tk ? e : bi; }
	v_mfma_f32_16x16x4_f32 v[66:69], v92, v221, v[66:69]
	v_mfma_f32_16x16x4_f32 v[70:73], v92, v222, v[70:73]
	v_mfma_f32_16x16x4_f32 v[66:69], v93, v223, v[66:69]
	v_mfma_f32_16x16x4_f32 v[70:73], v93, v224, v[70:73]
	v_mfma_f32_16x16x4_f32 v[66:69], v94, v225, v[66:69]
	v_mfma_f32_16x16x4_f32 v[70:73], v94, v226, v[70:73]
	v_mfma_f32_16x16x4_f32 v[66:69], v95, v227, v[66:69]
	v_mfma_f32_16x16x4_f32 v[70:73], v95, v228, v[70:73]
	s_waitcnt lgkmcnt(2)
	v_mfma_f32_16x16x4_f32 v[66:69], v96, v229, v[66:69]
	v_mfma_f32_16x16x4_f32 v[70:73], v96, v230, v[70:73]
	v_mfma_f32_16x16x4_f32 v[66:69], v97, v231, v[66:69]
	v_mfma_f32_16x16x4_f32 v[70:73], v97, v232, v[70:73]
	v_mfma_f32_16x16x4_f32 v[66:69], v98, v233, v[66:69]
	v_mfma_f32_16x16x4_f32 v[70:73], v98, v234, v[70:73]
	v_mfma_f32_16x16x4_f32 v[66:69], v99, v235, v[66:69]
	v_mfma_f32_16x16x4_f32 v[70:73], v99, v236, v[70:73]
	s_waitcnt lgkmcnt(1)
	v_mfma_f32_16x16x4_f32 v[66:69], v100, v237, v[66:69]
	v_mfma_f32_16x16x4_f32 v[70:73], v100, v238, v[70:73]
	v_mfma_f32_16x16x4_f32 v[66:69], v101, v239, v[66:69]
	v_mfma_f32_16x16x4_f32 v[70:73], v101, v240, v[70:73]
	v_mfma_f32_16x16x4_f32 v[66:69], v102, v241, v[66:69]
	v_mfma_f32_16x16x4_f32 v[70:73], v102, v242, v[70:73]
	v_mfma_f32_16x16x4_f32 v[66:69], v103, v243, v[66:69]
	v_mfma_f32_16x16x4_f32 v[70:73], v103, v244, v[70:73]
	s_waitcnt lgkmcnt(0)
	v_mfma_f32_16x16x4_f32 v[66:69], v104, v245, v[66:69]
	v_mfma_f32_16x16x4_f32 v[70:73], v104, v246, v[70:73]
	v_mfma_f32_16x16x4_f32 v[66:69], v105, v247, v[66:69]
	v_mfma_f32_16x16x4_f32 v[70:73], v105, v248, v[70:73]
	v_mfma_f32_16x16x4_f32 v[66:69], v106, v249, v[66:69]
	v_mfma_f32_16x16x4_f32 v[70:73], v106, v250, v[70:73]
	v_mfma_f32_16x16x4_f32 v[66:69], v107, v251, v[66:69]
	v_mfma_f32_16x16x4_f32 v[70:73], v107, v252, v[70:73]
	s_nop 8
	ds_write2_b32 v156, v66, v70 offset1:16
	ds_write2_b32 v156, v67, v71 offset0:32 offset1:48
	ds_write2_b32 v156, v68, v72 offset0:64 offset1:80
	ds_write2_b32 v156, v69, v73 offset0:96 offset1:112
	s_waitcnt lgkmcnt(0)
	s_barrier
	ds_read2st64_b32 v[66:67], v153 offset1:8
	ds_read2st64_b32 v[68:69], v153 offset0:16 offset1:24
	ds_read2st64_b32 v[70:71], v153 offset0:32 offset1:40
	ds_read2st64_b32 v[72:73], v153 offset0:48 offset1:56
	s_waitcnt lgkmcnt(3)
	v_add_f32_e32 v66, v253, v66
	v_add_f32_e32 v66, v66, v67
	s_waitcnt lgkmcnt(2)
	v_add_f32_e32 v66, v66, v68
	v_add_f32_e32 v66, v66, v69
	s_waitcnt lgkmcnt(1)
	v_add_f32_e32 v66, v66, v70
	v_add_f32_e32 v66, v66, v71
	s_waitcnt lgkmcnt(0)
	v_add_f32_e32 v66, v66, v72
	v_add_f32_e32 v66, v66, v73
	ds_write_b32 v154, v66
	s_waitcnt lgkmcnt(0)
	s_barrier
	s_and_saveexec_b64 s[0:1], s[4:5]
	s_cbranch_execz .LBB0_1513
	ds_read_b128 v[68:71], v157
	ds_read_b128 v[90:93], v157 offset:16
	ds_read_b128 v[94:97], v157 offset:32
	ds_read_b128 v[98:101], v157 offset:48
	ds_read_b128 v[102:105], v157 offset:64
	ds_read_b128 v[106:109], v157 offset:80
	ds_read_b128 v[110:113], v157 offset:96
	ds_read_b128 v[114:117], v157 offset:112
	s_waitcnt lgkmcnt(7)
	v_max_f32_e32 v66, v68, v68
	v_max_f32_e32 v66, 0xff7fc99e, v66
	v_cmp_gt_f32_e32 vcc, v69, v66
	s_nop 1
	v_cndmask_b32_e32 v66, v66, v69, vcc
	v_cndmask_b32_e64 v67, 0, 1, vcc
	v_cmp_gt_f32_e32 vcc, v70, v66
	s_nop 1
	v_cndmask_b32_e32 v66, v66, v70, vcc
	v_cndmask_b32_e64 v67, v67, 2, vcc
	v_cmp_gt_f32_e32 vcc, v71, v66
	s_nop 1
	v_cndmask_b32_e32 v66, v66, v71, vcc
	v_cndmask_b32_e64 v67, v67, 3, vcc
	s_waitcnt lgkmcnt(6)
	v_cmp_gt_f32_e32 vcc, v90, v66
	s_nop 1
	v_cndmask_b32_e32 v66, v66, v90, vcc
	v_cndmask_b32_e64 v67, v67, 4, vcc
	v_cmp_gt_f32_e32 vcc, v91, v66
	s_nop 1
	v_cndmask_b32_e32 v66, v66, v91, vcc
	v_cndmask_b32_e64 v67, v67, 5, vcc
	v_cmp_gt_f32_e32 vcc, v92, v66
	s_nop 1
	v_cndmask_b32_e32 v66, v66, v92, vcc
	v_cndmask_b32_e64 v67, v67, 6, vcc
	v_cmp_gt_f32_e32 vcc, v93, v66
	s_nop 1
	v_cndmask_b32_e32 v66, v66, v93, vcc
	v_cndmask_b32_e64 v67, v67, 7, vcc
	s_waitcnt lgkmcnt(5)
	v_cmp_gt_f32_e32 vcc, v94, v66
	s_nop 1
	v_cndmask_b32_e32 v66, v66, v94, vcc
	v_cndmask_b32_e64 v67, v67, 8, vcc
	v_cmp_gt_f32_e32 vcc, v95, v66
	s_nop 1
	v_cndmask_b32_e32 v66, v66, v95, vcc
	v_cndmask_b32_e64 v67, v67, 9, vcc
	v_cmp_gt_f32_e32 vcc, v96, v66
	s_nop 1
	v_cndmask_b32_e32 v66, v66, v96, vcc
	v_cndmask_b32_e64 v67, v67, 10, vcc
	v_cmp_gt_f32_e32 vcc, v97, v66
	s_nop 1
	v_cndmask_b32_e32 v66, v66, v97, vcc
	v_cndmask_b32_e64 v67, v67, 11, vcc
	s_waitcnt lgkmcnt(4)
	v_cmp_gt_f32_e32 vcc, v98, v66
	s_nop 1
	v_cndmask_b32_e32 v66, v66, v98, vcc
	v_cndmask_b32_e64 v67, v67, 12, vcc
	v_cmp_gt_f32_e32 vcc, v99, v66
	s_nop 1
	v_cndmask_b32_e32 v66, v66, v99, vcc
	v_cndmask_b32_e64 v67, v67, 13, vcc
	v_cmp_gt_f32_e32 vcc, v100, v66
	s_nop 1
	v_cndmask_b32_e32 v66, v66, v100, vcc
	v_cndmask_b32_e64 v67, v67, 14, vcc
	v_cmp_gt_f32_e32 vcc, v101, v66
	s_nop 1
	v_cndmask_b32_e32 v66, v66, v101, vcc
	v_cndmask_b32_e64 v67, v67, 15, vcc
	s_waitcnt lgkmcnt(3)
	v_cmp_gt_f32_e32 vcc, v102, v66
	s_nop 1
	v_cndmask_b32_e32 v66, v66, v102, vcc
	v_cndmask_b32_e64 v67, v67, 16, vcc
	v_cmp_gt_f32_e32 vcc, v103, v66
	s_nop 1
	v_cndmask_b32_e32 v66, v66, v103, vcc
	v_cndmask_b32_e64 v67, v67, 17, vcc
	v_cmp_gt_f32_e32 vcc, v104, v66
	s_nop 1
	v_cndmask_b32_e32 v66, v66, v104, vcc
	v_cndmask_b32_e64 v67, v67, 18, vcc
	v_cmp_gt_f32_e32 vcc, v105, v66
	s_nop 1
	v_cndmask_b32_e32 v66, v66, v105, vcc
	v_cndmask_b32_e64 v67, v67, 19, vcc
	s_waitcnt lgkmcnt(2)
; template <bool SKIP_MIX>
; __device__ __forceinline__ void p8_ln_router(Frame& F0, const In& I) {
;     ...
;             for (int k = 0; k < 4; ++k) { float best = -3.4e38f; int bi = 0;
; #pragma unroll
;                 for (int e = 0; e < 32; ++e) { const bool tk = lv[e] > best; best = tk ? lv[e] : best; bi = tk ? e : bi; }
;                 ti[k] = bi; tv[k] = best;
; #pragma unroll
;                 for (int e = 0; e < 32; ++e) lv[e] = (e == bi) ? -3.4e38f : lv[e]; }
	v_cmp_gt_f32_e32 vcc, v106, v66
	s_nop 1
	v_cndmask_b32_e32 v66, v66, v106, vcc
	v_cndmask_b32_e64 v67, v67, 20, vcc
	v_cmp_gt_f32_e32 vcc, v107, v66
	s_nop 1
	v_cndmask_b32_e32 v66, v66, v107, vcc
	v_cndmask_b32_e64 v67, v67, 21, vcc
	v_cmp_gt_f32_e32 vcc, v108, v66
	s_nop 1
	v_cndmask_b32_e32 v66, v66, v108, vcc
	v_cndmask_b32_e64 v67, v67, 22, vcc
	v_cmp_gt_f32_e32 vcc, v109, v66
	s_nop 1
	v_cndmask_b32_e32 v66, v66, v109, vcc
	v_cndmask_b32_e64 v67, v67, 23, vcc
	s_waitcnt lgkmcnt(1)
	v_cmp_gt_f32_e32 vcc, v110, v66
	s_nop 1
	v_cndmask_b32_e32 v66, v66, v110, vcc
	v_cndmask_b32_e64 v67, v67, 24, vcc
	v_cmp_gt_f32_e32 vcc, v111, v66
	s_nop 1
	v_cndmask_b32_e32 v66, v66, v111, vcc
	v_cndmask_b32_e64 v67, v67, 25, vcc
	v_cmp_gt_f32_e32 vcc, v112, v66
	s_nop 1
	v_cndmask_b32_e32 v66, v66, v112, vcc
	v_cndmask_b32_e64 v67, v67, 26, vcc
	v_cmp_gt_f32_e32 vcc, v113, v66
	s_nop 1
	v_cndmask_b32_e32 v66, v66, v113, vcc
	v_cndmask_b32_e64 v67, v67, 27, vcc
	s_waitcnt lgkmcnt(0)
	v_cmp_gt_f32_e32 vcc, v114, v66
	s_nop 1
	v_cndmask_b32_e32 v66, v66, v114, vcc
	v_cndmask_b32_e64 v67, v67, 28, vcc
	v_cmp_gt_f32_e32 vcc, v115, v66
	s_nop 1
	v_cndmask_b32_e32 v66, v66, v115, vcc
	v_cndmask_b32_e64 v67, v67, 29, vcc
	v_cmp_gt_f32_e32 vcc, v116, v66
	s_nop 1
	v_cndmask_b32_e32 v72, v66, v116, vcc
	v_cndmask_b32_e64 v67, v67, 30, vcc
	v_cmp_gt_f32_e32 vcc, v117, v72
	s_nop 1
	v_cndmask_b32_e64 v66, v67, 31, vcc
	v_cndmask_b32_e32 v73, v72, v117, vcc
	v_cmp_ne_u32_e32 vcc, 0, v66
	s_nop 1
	v_cndmask_b32_e32 v68, v159, v68, vcc
	v_cmp_ne_u32_e32 vcc, 1, v66
	v_max_f32_e32 v67, v68, v68
	v_max_f32_e32 v67, 0xff7fc99e, v67
	v_cndmask_b32_e32 v69, v159, v69, vcc
	v_cmp_ne_u32_e32 vcc, 2, v66
	s_nop 1
	v_cndmask_b32_e32 v70, v159, v70, vcc
	v_cmp_ne_u32_e32 vcc, 3, v66
	s_nop 1
	v_cndmask_b32_e32 v71, v159, v71, vcc
	v_cmp_ne_u32_e32 vcc, 4, v66
	s_nop 1
	v_cndmask_b32_e32 v72, v159, v90, vcc
	v_cmp_ne_u32_e32 vcc, 5, v66
	s_nop 1
	v_cndmask_b32_e32 v90, v159, v91, vcc
	v_cmp_ne_u32_e32 vcc, 6, v66
	s_nop 1
	v_cndmask_b32_e32 v91, v159, v92, vcc
	v_cmp_ne_u32_e32 vcc, 7, v66
	s_nop 1
	v_cndmask_b32_e32 v92, v159, v93, vcc
	v_cmp_ne_u32_e32 vcc, 8, v66
	s_nop 1
	v_cndmask_b32_e32 v93, v159, v94, vcc
	v_cmp_ne_u32_e32 vcc, 9, v66
	s_nop 1
	v_cndmask_b32_e32 v94, v159, v95, vcc
	v_cmp_ne_u32_e32 vcc, 10, v66
	s_nop 1
	v_cndmask_b32_e32 v95, v159, v96, vcc
	v_cmp_ne_u32_e32 vcc, 11, v66
	s_nop 1
	v_cndmask_b32_e32 v96, v159, v97, vcc
	v_cmp_ne_u32_e32 vcc, 12, v66
	s_nop 1
	v_cndmask_b32_e32 v97, v159, v98, vcc
	v_cmp_ne_u32_e32 vcc, 13, v66
	s_nop 1
	v_cndmask_b32_e32 v98, v159, v99, vcc
	v_cmp_ne_u32_e32 vcc, 14, v66
	s_nop 1
	v_cndmask_b32_e32 v99, v159, v100, vcc
	v_cmp_ne_u32_e32 vcc, 15, v66
	s_nop 1
	v_cndmask_b32_e32 v100, v159, v101, vcc
	v_cmp_ne_u32_e32 vcc, 16, v66
	s_nop 1
	v_cndmask_b32_e32 v101, v159, v102, vcc
	v_cmp_ne_u32_e32 vcc, 17, v66
	s_nop 1
	v_cndmask_b32_e32 v102, v159, v103, vcc
	v_cmp_ne_u32_e32 vcc, 18, v66
	s_nop 1
	v_cndmask_b32_e32 v103, v159, v104, vcc
	v_cmp_ne_u32_e32 vcc, 19, v66
	s_nop 1
	v_cndmask_b32_e32 v104, v159, v105, vcc
	v_cmp_ne_u32_e32 vcc, 20, v66
	s_nop 1
	v_cndmask_b32_e32 v105, v159, v106, vcc
	v_cmp_ne_u32_e32 vcc, 21, v66
	s_nop 1
	v_cndmask_b32_e32 v106, v159, v107, vcc
	v_cmp_ne_u32_e32 vcc, 22, v66
	s_nop 1
	v_cndmask_b32_e32 v107, v159, v108, vcc
	v_cmp_ne_u32_e32 vcc, 23, v66
	s_nop 1
	v_cndmask_b32_e32 v108, v159, v109, vcc
	v_cmp_ne_u32_e32 vcc, 24, v66
	s_nop 1
	v_cndmask_b32_e32 v109, v159, v110, vcc
	v_cmp_ne_u32_e32 vcc, 25, v66
	s_nop 1
	v_cndmask_b32_e32 v110, v159, v111, vcc
	v_cmp_ne_u32_e32 vcc, 26, v66
	s_nop 1
	v_cndmask_b32_e32 v111, v159, v112, vcc
	v_cmp_ne_u32_e32 vcc, 27, v66
	s_nop 1
	v_cndmask_b32_e32 v112, v159, v113, vcc
	v_cmp_ne_u32_e32 vcc, 28, v66
	s_nop 1
	v_cndmask_b32_e32 v113, v159, v114, vcc
	v_cmp_ne_u32_e32 vcc, 29, v66
	s_nop 1
	v_cndmask_b32_e32 v114, v159, v115, vcc
	v_cmp_ne_u32_e32 vcc, 30, v66
	s_nop 1
	v_cndmask_b32_e32 v115, v159, v116, vcc
	v_cmp_ne_u32_e32 vcc, 31, v66
	s_nop 1
	v_cndmask_b32_e32 v116, v159, v117, vcc
	v_cmp_gt_f32_e32 vcc, v69, v67
	s_nop 1
	v_cndmask_b32_e32 v67, v67, v69, vcc
	v_cndmask_b32_e64 v117, 0, 1, vcc
	v_cmp_gt_f32_e32 vcc, v70, v67
	s_nop 1
	v_cndmask_b32_e32 v67, v67, v70, vcc
	v_cndmask_b32_e64 v117, v117, 2, vcc
	v_cmp_gt_f32_e32 vcc, v71, v67
	s_nop 1
	v_cndmask_b32_e32 v67, v67, v71, vcc
	v_cndmask_b32_e64 v117, v117, 3, vcc
	v_cmp_gt_f32_e32 vcc, v72, v67
	s_nop 1
	v_cndmask_b32_e32 v67, v67, v72, vcc
	v_cndmask_b32_e64 v117, v117, 4, vcc
	v_cmp_gt_f32_e32 vcc, v90, v67
	s_nop 1
	v_cndmask_b32_e32 v67, v67, v90, vcc
	v_cndmask_b32_e64 v117, v117, 5, vcc
	v_cmp_gt_f32_e32 vcc, v91, v67
	s_nop 1
	v_cndmask_b32_e32 v67, v67, v91, vcc
	v_cndmask_b32_e64 v117, v117, 6, vcc
	v_cmp_gt_f32_e32 vcc, v92, v67
	s_nop 1
	v_cndmask_b32_e32 v67, v67, v92, vcc
	v_cndmask_b32_e64 v117, v117, 7, vcc
	v_cmp_gt_f32_e32 vcc, v93, v67
	s_nop 1
	v_cndmask_b32_e32 v67, v67, v93, vcc
	v_cndmask_b32_e64 v117, v117, 8, vcc
	v_cmp_gt_f32_e32 vcc, v94, v67
	s_nop 1
	v_cndmask_b32_e32 v67, v67, v94, vcc
	v_cndmask_b32_e64 v117, v117, 9, vcc
	v_cmp_gt_f32_e32 vcc, v95, v67
	s_nop 1
	v_cndmask_b32_e32 v67, v67, v95, vcc
	v_cndmask_b32_e64 v117, v117, 10, vcc
	v_cmp_gt_f32_e32 vcc, v96, v67
	s_nop 1
	v_cndmask_b32_e32 v67, v67, v96, vcc
	v_cndmask_b32_e64 v117, v117, 11, vcc
	v_cmp_gt_f32_e32 vcc, v97, v67
	s_nop 1
	v_cndmask_b32_e32 v67, v67, v97, vcc
	v_cndmask_b32_e64 v117, v117, 12, vcc
	v_cmp_gt_f32_e32 vcc, v98, v67
	s_nop 1
	v_cndmask_b32_e32 v67, v67, v98, vcc
	v_cndmask_b32_e64 v117, v117, 13, vcc
	v_cmp_gt_f32_e32 vcc, v99, v67
	s_nop 1
; template <bool SKIP_MIX>
; __device__ __forceinline__ void p8_ln_router(Frame& F0, const In& I) {
;     ...
;             for (int k = 0; k < 4; ++k) { float best = -3.4e38f; int bi = 0;
; #pragma unroll
;                 for (int e = 0; e < 32; ++e) { const bool tk = lv[e] > best; best = tk ? lv[e] : best; bi = tk ? e : bi; }
;                 ti[k] = bi; tv[k] = best;
; #pragma unroll
;                 for (int e = 0; e < 32; ++e) lv[e] = (e == bi) ? -3.4e38f : lv[e]; }
	v_cndmask_b32_e32 v67, v67, v99, vcc
	v_cndmask_b32_e64 v117, v117, 14, vcc
	v_cmp_gt_f32_e32 vcc, v100, v67
	s_nop 1
	v_cndmask_b32_e32 v67, v67, v100, vcc
	v_cndmask_b32_e64 v117, v117, 15, vcc
	v_cmp_gt_f32_e32 vcc, v101, v67
	s_nop 1
	v_cndmask_b32_e32 v67, v67, v101, vcc
	v_cndmask_b32_e64 v117, v117, 16, vcc
	v_cmp_gt_f32_e32 vcc, v102, v67
	s_nop 1
	v_cndmask_b32_e32 v67, v67, v102, vcc
	v_cndmask_b32_e64 v117, v117, 17, vcc
	v_cmp_gt_f32_e32 vcc, v103, v67
	s_nop 1
	v_cndmask_b32_e32 v67, v67, v103, vcc
	v_cndmask_b32_e64 v117, v117, 18, vcc
	v_cmp_gt_f32_e32 vcc, v104, v67
	s_nop 1
	v_cndmask_b32_e32 v67, v67, v104, vcc
	v_cndmask_b32_e64 v117, v117, 19, vcc
	v_cmp_gt_f32_e32 vcc, v105, v67
	s_nop 1
	v_cndmask_b32_e32 v67, v67, v105, vcc
	v_cndmask_b32_e64 v117, v117, 20, vcc
	v_cmp_gt_f32_e32 vcc, v106, v67
	s_nop 1
	v_cndmask_b32_e32 v67, v67, v106, vcc
	v_cndmask_b32_e64 v117, v117, 21, vcc
	v_cmp_gt_f32_e32 vcc, v107, v67
	s_nop 1
	v_cndmask_b32_e32 v67, v67, v107, vcc
	v_cndmask_b32_e64 v117, v117, 22, vcc
	v_cmp_gt_f32_e32 vcc, v108, v67
	s_nop 1
	v_cndmask_b32_e32 v67, v67, v108, vcc
	v_cndmask_b32_e64 v117, v117, 23, vcc
	v_cmp_gt_f32_e32 vcc, v109, v67
	s_nop 1
	v_cndmask_b32_e32 v67, v67, v109, vcc
	v_cndmask_b32_e64 v117, v117, 24, vcc
	v_cmp_gt_f32_e32 vcc, v110, v67
	s_nop 1
	v_cndmask_b32_e32 v67, v67, v110, vcc
	v_cndmask_b32_e64 v117, v117, 25, vcc
	v_cmp_gt_f32_e32 vcc, v111, v67
	s_nop 1
	v_cndmask_b32_e32 v67, v67, v111, vcc
	v_cndmask_b32_e64 v117, v117, 26, vcc
	v_cmp_gt_f32_e32 vcc, v112, v67
	s_nop 1
	v_cndmask_b32_e32 v67, v67, v112, vcc
	v_cndmask_b32_e64 v117, v117, 27, vcc
	v_cmp_gt_f32_e32 vcc, v113, v67
	s_nop 1
	v_cndmask_b32_e32 v67, v67, v113, vcc
	v_cndmask_b32_e64 v117, v117, 28, vcc
	v_cmp_gt_f32_e32 vcc, v114, v67
	s_nop 1
	v_cndmask_b32_e32 v67, v67, v114, vcc
	v_cndmask_b32_e64 v117, v117, 29, vcc
	v_cmp_gt_f32_e32 vcc, v115, v67
	s_nop 1
	v_cndmask_b32_e32 v118, v67, v115, vcc
	v_cndmask_b32_e64 v117, v117, 30, vcc
	v_cmp_gt_f32_e32 vcc, v116, v118
	s_nop 1
	v_cndmask_b32_e64 v67, v117, 31, vcc
	v_cndmask_b32_e32 v117, v118, v116, vcc
	v_cmp_ne_u32_e32 vcc, 0, v67
	s_nop 1
	v_cndmask_b32_e32 v118, v159, v68, vcc
	v_cmp_ne_u32_e32 vcc, 1, v67
	v_max_f32_e32 v68, v118, v118
	v_max_f32_e32 v68, 0xff7fc99e, v68
	v_cndmask_b32_e32 v69, v159, v69, vcc
	v_cmp_ne_u32_e32 vcc, 2, v67
	s_nop 1
	v_cndmask_b32_e32 v70, v159, v70, vcc
	v_cmp_ne_u32_e32 vcc, 3, v67
	s_nop 1
	v_cndmask_b32_e32 v71, v159, v71, vcc
	v_cmp_ne_u32_e32 vcc, 4, v67
	s_nop 1
	v_cndmask_b32_e32 v72, v159, v72, vcc
	v_cmp_ne_u32_e32 vcc, 5, v67
	s_nop 1
	v_cndmask_b32_e32 v90, v159, v90, vcc
	v_cmp_ne_u32_e32 vcc, 6, v67
	s_nop 1
	v_cndmask_b32_e32 v91, v159, v91, vcc
	v_cmp_ne_u32_e32 vcc, 7, v67
	s_nop 1
	v_cndmask_b32_e32 v92, v159, v92, vcc
	v_cmp_ne_u32_e32 vcc, 8, v67
	s_nop 1
	v_cndmask_b32_e32 v93, v159, v93, vcc
	v_cmp_ne_u32_e32 vcc, 9, v67
	s_nop 1
	v_cndmask_b32_e32 v94, v159, v94, vcc
	v_cmp_ne_u32_e32 vcc, 10, v67
	s_nop 1
	v_cndmask_b32_e32 v95, v159, v95, vcc
	v_cmp_ne_u32_e32 vcc, 11, v67
	s_nop 1
	v_cndmask_b32_e32 v96, v159, v96, vcc
	v_cmp_ne_u32_e32 vcc, 12, v67
	s_nop 1
	v_cndmask_b32_e32 v97, v159, v97, vcc
	v_cmp_ne_u32_e32 vcc, 13, v67
	s_nop 1
	v_cndmask_b32_e32 v98, v159, v98, vcc
	v_cmp_ne_u32_e32 vcc, 14, v67
	s_nop 1
	v_cndmask_b32_e32 v99, v159, v99, vcc
	v_cmp_ne_u32_e32 vcc, 15, v67
	s_nop 1
	v_cndmask_b32_e32 v100, v159, v100, vcc
	v_cmp_ne_u32_e32 vcc, 16, v67
	s_nop 1
	v_cndmask_b32_e32 v101, v159, v101, vcc
	v_cmp_ne_u32_e32 vcc, 17, v67
	s_nop 1
	v_cndmask_b32_e32 v102, v159, v102, vcc
	v_cmp_ne_u32_e32 vcc, 18, v67
	s_nop 1
	v_cndmask_b32_e32 v103, v159, v103, vcc
	v_cmp_ne_u32_e32 vcc, 19, v67
	s_nop 1
	v_cndmask_b32_e32 v104, v159, v104, vcc
	v_cmp_ne_u32_e32 vcc, 20, v67
	s_nop 1
	v_cndmask_b32_e32 v105, v159, v105, vcc
	v_cmp_ne_u32_e32 vcc, 21, v67
	s_nop 1
	v_cndmask_b32_e32 v106, v159, v106, vcc
	v_cmp_ne_u32_e32 vcc, 22, v67
	s_nop 1
	v_cndmask_b32_e32 v107, v159, v107, vcc
	v_cmp_ne_u32_e32 vcc, 23, v67
	s_nop 1
	v_cndmask_b32_e32 v108, v159, v108, vcc
	v_cmp_ne_u32_e32 vcc, 24, v67
	s_nop 1
	v_cndmask_b32_e32 v109, v159, v109, vcc
	v_cmp_ne_u32_e32 vcc, 25, v67
	s_nop 1
	v_cndmask_b32_e32 v110, v159, v110, vcc
	v_cmp_ne_u32_e32 vcc, 26, v67
	s_nop 1
	v_cndmask_b32_e32 v111, v159, v111, vcc
	v_cmp_ne_u32_e32 vcc, 27, v67
	s_nop 1
	v_cndmask_b32_e32 v112, v159, v112, vcc
	v_cmp_ne_u32_e32 vcc, 28, v67
	s_nop 1
	v_cndmask_b32_e32 v113, v159, v113, vcc
	v_cmp_ne_u32_e32 vcc, 29, v67
	s_nop 1
	v_cndmask_b32_e32 v114, v159, v114, vcc
	v_cmp_ne_u32_e32 vcc, 30, v67
	s_nop 1
	v_cndmask_b32_e32 v115, v159, v115, vcc
	v_cmp_ne_u32_e32 vcc, 31, v67
	s_nop 1
	v_cndmask_b32_e32 v116, v159, v116, vcc
	v_cmp_gt_f32_e32 vcc, v69, v68
	s_nop 1
	v_cndmask_b32_e32 v68, v68, v69, vcc
	v_cndmask_b32_e64 v119, 0, 1, vcc
	v_cmp_gt_f32_e32 vcc, v70, v68
	s_nop 1
	v_cndmask_b32_e32 v68, v68, v70, vcc
	v_cndmask_b32_e64 v119, v119, 2, vcc
	v_cmp_gt_f32_e32 vcc, v71, v68
	s_nop 1
	v_cndmask_b32_e32 v68, v68, v71, vcc
	v_cndmask_b32_e64 v119, v119, 3, vcc
	v_cmp_gt_f32_e32 vcc, v72, v68
	s_nop 1
	v_cndmask_b32_e32 v68, v68, v72, vcc
	v_cndmask_b32_e64 v119, v119, 4, vcc
	v_cmp_gt_f32_e32 vcc, v90, v68
	s_nop 1
	v_cndmask_b32_e32 v68, v68, v90, vcc
	v_cndmask_b32_e64 v119, v119, 5, vcc
	v_cmp_gt_f32_e32 vcc, v91, v68
	s_nop 1
	v_cndmask_b32_e32 v68, v68, v91, vcc
	v_cndmask_b32_e64 v119, v119, 6, vcc
	v_cmp_gt_f32_e32 vcc, v92, v68
	s_nop 1
	v_cndmask_b32_e32 v68, v68, v92, vcc
	v_cndmask_b32_e64 v119, v119, 7, vcc
	v_cmp_gt_f32_e32 vcc, v93, v68
	s_nop 1
	v_cndmask_b32_e32 v68, v68, v93, vcc
; template <bool SKIP_MIX>
; __device__ __forceinline__ void p8_ln_router(Frame& F0, const In& I) {
;     ...
;             for (int k = 0; k < 4; ++k) { float best = -3.4e38f; int bi = 0;
; #pragma unroll
;                 for (int e = 0; e < 32; ++e) { const bool tk = lv[e] > best; best = tk ? lv[e] : best; bi = tk ? e : bi; }
;                 ti[k] = bi; tv[k] = best;
; #pragma unroll
;                 for (int e = 0; e < 32; ++e) lv[e] = (e == bi) ? -3.4e38f : lv[e]; }
	v_cndmask_b32_e64 v119, v119, 8, vcc
	v_cmp_gt_f32_e32 vcc, v94, v68
	s_nop 1
	v_cndmask_b32_e32 v68, v68, v94, vcc
	v_cndmask_b32_e64 v119, v119, 9, vcc
	v_cmp_gt_f32_e32 vcc, v95, v68
	s_nop 1
	v_cndmask_b32_e32 v68, v68, v95, vcc
	v_cndmask_b32_e64 v119, v119, 10, vcc
	v_cmp_gt_f32_e32 vcc, v96, v68
	s_nop 1
	v_cndmask_b32_e32 v68, v68, v96, vcc
	v_cndmask_b32_e64 v119, v119, 11, vcc
	v_cmp_gt_f32_e32 vcc, v97, v68
	s_nop 1
	v_cndmask_b32_e32 v68, v68, v97, vcc
	v_cndmask_b32_e64 v119, v119, 12, vcc
	v_cmp_gt_f32_e32 vcc, v98, v68
	s_nop 1
	v_cndmask_b32_e32 v68, v68, v98, vcc
	v_cndmask_b32_e64 v119, v119, 13, vcc
	v_cmp_gt_f32_e32 vcc, v99, v68
	s_nop 1
	v_cndmask_b32_e32 v68, v68, v99, vcc
	v_cndmask_b32_e64 v119, v119, 14, vcc
	v_cmp_gt_f32_e32 vcc, v100, v68
	s_nop 1
	v_cndmask_b32_e32 v68, v68, v100, vcc
	v_cndmask_b32_e64 v119, v119, 15, vcc
	v_cmp_gt_f32_e32 vcc, v101, v68
	s_nop 1
	v_cndmask_b32_e32 v68, v68, v101, vcc
	v_cndmask_b32_e64 v119, v119, 16, vcc
	v_cmp_gt_f32_e32 vcc, v102, v68
	s_nop 1
	v_cndmask_b32_e32 v68, v68, v102, vcc
	v_cndmask_b32_e64 v119, v119, 17, vcc
	v_cmp_gt_f32_e32 vcc, v103, v68
	s_nop 1
	v_cndmask_b32_e32 v68, v68, v103, vcc
	v_cndmask_b32_e64 v119, v119, 18, vcc
	v_cmp_gt_f32_e32 vcc, v104, v68
	s_nop 1
	v_cndmask_b32_e32 v68, v68, v104, vcc
	v_cndmask_b32_e64 v119, v119, 19, vcc
	v_cmp_gt_f32_e32 vcc, v105, v68
	s_nop 1
	v_cndmask_b32_e32 v68, v68, v105, vcc
	v_cndmask_b32_e64 v119, v119, 20, vcc
	v_cmp_gt_f32_e32 vcc, v106, v68
	s_nop 1
	v_cndmask_b32_e32 v68, v68, v106, vcc
	v_cndmask_b32_e64 v119, v119, 21, vcc
	v_cmp_gt_f32_e32 vcc, v107, v68
	s_nop 1
	v_cndmask_b32_e32 v68, v68, v107, vcc
	v_cndmask_b32_e64 v119, v119, 22, vcc
	v_cmp_gt_f32_e32 vcc, v108, v68
	s_nop 1
	v_cndmask_b32_e32 v68, v68, v108, vcc
	v_cndmask_b32_e64 v119, v119, 23, vcc
	v_cmp_gt_f32_e32 vcc, v109, v68
	s_nop 1
	v_cndmask_b32_e32 v68, v68, v109, vcc
	v_cndmask_b32_e64 v119, v119, 24, vcc
	v_cmp_gt_f32_e32 vcc, v110, v68
	s_nop 1
	v_cndmask_b32_e32 v68, v68, v110, vcc
	v_cndmask_b32_e64 v119, v119, 25, vcc
	v_cmp_gt_f32_e32 vcc, v111, v68
	s_nop 1
	v_cndmask_b32_e32 v68, v68, v111, vcc
	v_cndmask_b32_e64 v119, v119, 26, vcc
	v_cmp_gt_f32_e32 vcc, v112, v68
	s_nop 1
	v_cndmask_b32_e32 v68, v68, v112, vcc
	v_cndmask_b32_e64 v119, v119, 27, vcc
	v_cmp_gt_f32_e32 vcc, v113, v68
	s_nop 1
	v_cndmask_b32_e32 v68, v68, v113, vcc
	v_cndmask_b32_e64 v119, v119, 28, vcc
	v_cmp_gt_f32_e32 vcc, v114, v68
	s_nop 1
	v_cndmask_b32_e32 v68, v68, v114, vcc
	v_cndmask_b32_e64 v119, v119, 29, vcc
	v_cmp_gt_f32_e32 vcc, v115, v68
	s_nop 1
	v_cndmask_b32_e32 v120, v68, v115, vcc
	v_cndmask_b32_e64 v119, v119, 30, vcc
	v_cmp_gt_f32_e32 vcc, v116, v120
	s_nop 1
	v_cndmask_b32_e64 v68, v119, 31, vcc
	v_cndmask_b32_e32 v119, v120, v116, vcc
	v_cmp_ne_u32_e32 vcc, 0, v68
	s_nop 1
	v_cndmask_b32_e32 v118, v159, v118, vcc
	v_cmp_ne_u32_e32 vcc, 1, v68
	v_max_f32_e32 v118, v118, v118
	v_max_f32_e32 v118, 0xff7fc99e, v118
	v_cndmask_b32_e32 v69, v159, v69, vcc
	v_cmp_ne_u32_e32 vcc, 2, v68
	s_nop 1
	v_cndmask_b32_e32 v70, v159, v70, vcc
	v_cmp_ne_u32_e32 vcc, 3, v68
	s_nop 1
	v_cndmask_b32_e32 v71, v159, v71, vcc
	v_cmp_ne_u32_e32 vcc, 4, v68
	s_nop 1
	v_cndmask_b32_e32 v72, v159, v72, vcc
	v_cmp_ne_u32_e32 vcc, 5, v68
	s_nop 1
	v_cndmask_b32_e32 v90, v159, v90, vcc
	v_cmp_ne_u32_e32 vcc, 6, v68
	s_nop 1
	v_cndmask_b32_e32 v91, v159, v91, vcc
	v_cmp_ne_u32_e32 vcc, 7, v68
	s_nop 1
	v_cndmask_b32_e32 v92, v159, v92, vcc
	v_cmp_ne_u32_e32 vcc, 8, v68
	s_nop 1
	v_cndmask_b32_e32 v93, v159, v93, vcc
	v_cmp_ne_u32_e32 vcc, 9, v68
	s_nop 1
	v_cndmask_b32_e32 v94, v159, v94, vcc
	v_cmp_ne_u32_e32 vcc, 10, v68
	s_nop 1
	v_cndmask_b32_e32 v95, v159, v95, vcc
	v_cmp_ne_u32_e32 vcc, 11, v68
	s_nop 1
	v_cndmask_b32_e32 v96, v159, v96, vcc
	v_cmp_ne_u32_e32 vcc, 12, v68
	s_nop 1
	v_cndmask_b32_e32 v97, v159, v97, vcc
	v_cmp_ne_u32_e32 vcc, 13, v68
	s_nop 1
	v_cndmask_b32_e32 v98, v159, v98, vcc
	v_cmp_ne_u32_e32 vcc, 14, v68
	s_nop 1
	v_cndmask_b32_e32 v99, v159, v99, vcc
	v_cmp_ne_u32_e32 vcc, 15, v68
	s_nop 1
	v_cndmask_b32_e32 v100, v159, v100, vcc
	v_cmp_ne_u32_e32 vcc, 16, v68
	s_nop 1
	v_cndmask_b32_e32 v101, v159, v101, vcc
	v_cmp_ne_u32_e32 vcc, 17, v68
	s_nop 1
	v_cndmask_b32_e32 v102, v159, v102, vcc
	v_cmp_ne_u32_e32 vcc, 18, v68
	s_nop 1
	v_cndmask_b32_e32 v103, v159, v103, vcc
	v_cmp_ne_u32_e32 vcc, 19, v68
	s_nop 1
	v_cndmask_b32_e32 v104, v159, v104, vcc
	v_cmp_ne_u32_e32 vcc, 20, v68
	s_nop 1
	v_cndmask_b32_e32 v105, v159, v105, vcc
	v_cmp_ne_u32_e32 vcc, 21, v68
	s_nop 1
	v_cndmask_b32_e32 v106, v159, v106, vcc
	v_cmp_ne_u32_e32 vcc, 22, v68
	s_nop 1
	v_cndmask_b32_e32 v107, v159, v107, vcc
	v_cmp_ne_u32_e32 vcc, 23, v68
	s_nop 1
	v_cndmask_b32_e32 v108, v159, v108, vcc
	v_cmp_ne_u32_e32 vcc, 24, v68
	s_nop 1
	v_cndmask_b32_e32 v109, v159, v109, vcc
	v_cmp_ne_u32_e32 vcc, 25, v68
	s_nop 1
	v_cndmask_b32_e32 v110, v159, v110, vcc
	v_cmp_ne_u32_e32 vcc, 26, v68
	s_nop 1
	v_cndmask_b32_e32 v111, v159, v111, vcc
	v_cmp_ne_u32_e32 vcc, 27, v68
	s_nop 1
	v_cndmask_b32_e32 v112, v159, v112, vcc
	v_cmp_ne_u32_e32 vcc, 28, v68
	s_nop 1
	v_cndmask_b32_e32 v113, v159, v113, vcc
	v_cmp_ne_u32_e32 vcc, 29, v68
	s_nop 1
	v_cndmask_b32_e32 v114, v159, v114, vcc
	v_cmp_ne_u32_e32 vcc, 30, v68
; #define GAS __attribute__((address_space(1)))
; template <bool SKIP_MIX>
; __device__ __forceinline__ void p8_ln_router(Frame& F0, const In& I) {
;     ...
;             for (int k = 0; k < 4; ++k) { float best = -3.4e38f; int bi = 0;
; #pragma unroll
;                 for (int e = 0; e < 32; ++e) { const bool tk = lv[e] > best; best = tk ? lv[e] : best; bi = tk ? e : bi; }
;                 ti[k] = bi; tv[k] = best;
; #pragma unroll
;                 for (int e = 0; e < 32; ++e) lv[e] = (e == bi) ? -3.4e38f : lv[e]; }
;             float ex[4], sum = 0.f;
; #pragma unroll
;             for (int k = 0; k < 4; ++k) { ex[k] = __expf(tv[k] - tv[0]); sum += ex[k]; }
;             const float inv = 1.f / sum;
;             *(GAS v4u*)((int*)(F.ws + WS_TOPI) + (size_t)(tok0 + tl) * 4) = (v4u){(unsigned)ti[0], (unsigned)ti[1], (unsigned)ti[2], (unsigned)ti[3]};
;             *(GAS f32x4*)((float*)(F.ws + WS_GATE) + (size_t)(tok0 + tl) * 4) = (f32x4){ex[0] * inv, ex[1] * inv, ex[2] * inv, ex[3] * inv};
; #pragma unroll
;             for (int k = 0; k < 4; ++k) __hip_atomic_fetch_add(&hist[ti[k]], 1, __ATOMIC_RELAXED, __HIP_MEMORY_SCOPE_WORKGROUP);
	s_nop 1
	v_cndmask_b32_e32 v115, v159, v115, vcc
	v_cmp_ne_u32_e32 vcc, 31, v68
	s_nop 1
	v_cndmask_b32_e32 v116, v159, v116, vcc
	v_cmp_gt_f32_e32 vcc, v69, v118
	s_nop 1
	v_cndmask_b32_e32 v69, v118, v69, vcc
	v_cndmask_b32_e64 v120, 0, 1, vcc
	v_cmp_gt_f32_e32 vcc, v70, v69
	s_nop 1
	v_cndmask_b32_e32 v69, v69, v70, vcc
	v_cndmask_b32_e64 v118, v120, 2, vcc
	v_cmp_gt_f32_e32 vcc, v71, v69
	s_nop 1
	v_cndmask_b32_e32 v69, v69, v71, vcc
	v_cndmask_b32_e64 v70, v118, 3, vcc
	v_cmp_gt_f32_e32 vcc, v72, v69
	s_nop 1
	v_cndmask_b32_e32 v69, v69, v72, vcc
	v_cndmask_b32_e64 v70, v70, 4, vcc
	v_cmp_gt_f32_e32 vcc, v90, v69
	v_sub_f32_e32 v72, v119, v73
	v_mul_f32_e32 v72, 0x3fb8aa3b, v72
	v_cndmask_b32_e32 v69, v69, v90, vcc
	v_cndmask_b32_e64 v70, v70, 5, vcc
	v_cmp_gt_f32_e32 vcc, v91, v69
	v_exp_f32_e32 v72, v72
	s_nop 0
	v_cndmask_b32_e32 v69, v69, v91, vcc
	v_cndmask_b32_e64 v70, v70, 6, vcc
	v_cmp_gt_f32_e32 vcc, v92, v69
	s_nop 1
	v_cndmask_b32_e32 v69, v69, v92, vcc
	v_cndmask_b32_e64 v70, v70, 7, vcc
	v_cmp_gt_f32_e32 vcc, v93, v69
	s_nop 1
	v_cndmask_b32_e32 v69, v69, v93, vcc
	v_cndmask_b32_e64 v70, v70, 8, vcc
	v_cmp_gt_f32_e32 vcc, v94, v69
	s_nop 1
	v_cndmask_b32_e32 v69, v69, v94, vcc
	v_cndmask_b32_e64 v70, v70, 9, vcc
	v_cmp_gt_f32_e32 vcc, v95, v69
	s_nop 1
	v_cndmask_b32_e32 v69, v69, v95, vcc
	v_cndmask_b32_e64 v70, v70, 10, vcc
	v_cmp_gt_f32_e32 vcc, v96, v69
	s_nop 1
	v_cndmask_b32_e32 v69, v69, v96, vcc
	v_cndmask_b32_e64 v70, v70, 11, vcc
	v_cmp_gt_f32_e32 vcc, v97, v69
	s_nop 1
	v_cndmask_b32_e32 v69, v69, v97, vcc
	v_cndmask_b32_e64 v70, v70, 12, vcc
	v_cmp_gt_f32_e32 vcc, v98, v69
	s_nop 1
	v_cndmask_b32_e32 v69, v69, v98, vcc
	v_cndmask_b32_e64 v70, v70, 13, vcc
	v_cmp_gt_f32_e32 vcc, v99, v69
	s_nop 1
	v_cndmask_b32_e32 v69, v69, v99, vcc
	v_cndmask_b32_e64 v70, v70, 14, vcc
	v_cmp_gt_f32_e32 vcc, v100, v69
	s_nop 1
	v_cndmask_b32_e32 v69, v69, v100, vcc
	v_cndmask_b32_e64 v70, v70, 15, vcc
	v_cmp_gt_f32_e32 vcc, v101, v69
	s_nop 1
	v_cndmask_b32_e32 v69, v69, v101, vcc
	v_cndmask_b32_e64 v70, v70, 16, vcc
	v_cmp_gt_f32_e32 vcc, v102, v69
	s_nop 1
	v_cndmask_b32_e32 v69, v69, v102, vcc
	v_cndmask_b32_e64 v70, v70, 17, vcc
	v_cmp_gt_f32_e32 vcc, v103, v69
	s_nop 1
	v_cndmask_b32_e32 v69, v69, v103, vcc
	v_cndmask_b32_e64 v70, v70, 18, vcc
	v_cmp_gt_f32_e32 vcc, v104, v69
	s_nop 1
	v_cndmask_b32_e32 v69, v69, v104, vcc
	v_cndmask_b32_e64 v70, v70, 19, vcc
	v_cmp_gt_f32_e32 vcc, v105, v69
	s_nop 1
	v_cndmask_b32_e32 v69, v69, v105, vcc
	v_cndmask_b32_e64 v70, v70, 20, vcc
	v_cmp_gt_f32_e32 vcc, v106, v69
	s_nop 1
	v_cndmask_b32_e32 v69, v69, v106, vcc
	v_cndmask_b32_e64 v70, v70, 21, vcc
	v_cmp_gt_f32_e32 vcc, v107, v69
	s_nop 1
	v_cndmask_b32_e32 v69, v69, v107, vcc
	v_cndmask_b32_e64 v70, v70, 22, vcc
	v_cmp_gt_f32_e32 vcc, v108, v69
	s_nop 1
	v_cndmask_b32_e32 v69, v69, v108, vcc
	v_cndmask_b32_e64 v70, v70, 23, vcc
	v_cmp_gt_f32_e32 vcc, v109, v69
	s_nop 1
	v_cndmask_b32_e32 v69, v69, v109, vcc
	v_cndmask_b32_e64 v70, v70, 24, vcc
	v_cmp_gt_f32_e32 vcc, v110, v69
	s_nop 1
	v_cndmask_b32_e32 v69, v69, v110, vcc
	v_cndmask_b32_e64 v70, v70, 25, vcc
	v_cmp_gt_f32_e32 vcc, v111, v69
	s_nop 1
	v_cndmask_b32_e32 v69, v69, v111, vcc
	v_cndmask_b32_e64 v70, v70, 26, vcc
	v_cmp_gt_f32_e32 vcc, v112, v69
	s_nop 1
	v_cndmask_b32_e32 v69, v69, v112, vcc
	v_cndmask_b32_e64 v70, v70, 27, vcc
	v_cmp_gt_f32_e32 vcc, v113, v69
	s_nop 1
	v_cndmask_b32_e32 v69, v69, v113, vcc
	v_cndmask_b32_e64 v70, v70, 28, vcc
	v_cmp_gt_f32_e32 vcc, v114, v69
	s_nop 1
	v_cndmask_b32_e32 v69, v69, v114, vcc
	v_cndmask_b32_e64 v70, v70, 29, vcc
	v_cmp_gt_f32_e32 vcc, v115, v69
	s_nop 1
	v_cndmask_b32_e32 v71, v69, v115, vcc
	v_cndmask_b32_e64 v70, v70, 30, vcc
	v_cmp_gt_f32_e32 vcc, v116, v71
	s_nop 1
	v_cndmask_b32_e64 v69, v70, 31, vcc
	v_sub_f32_e32 v70, v73, v73
	v_cndmask_b32_e32 v90, v71, v116, vcc
	v_mul_f32_e32 v70, 0x3fb8aa3b, v70
	v_sub_f32_e32 v71, v117, v73
	v_exp_f32_e32 v70, v70
	v_mul_f32_e32 v71, 0x3fb8aa3b, v71
	v_exp_f32_e32 v71, v71
	v_sub_f32_e32 v73, v90, v73
	v_mul_f32_e32 v73, 0x3fb8aa3b, v73
	v_exp_f32_e32 v73, v73
	v_add_f32_e32 v90, 0, v70
	v_add_f32_e32 v90, v90, v71
	v_add_f32_e32 v90, v90, v72
	v_add_f32_e32 v90, v90, v73
	v_div_scale_f32 v91, s[14:15], v90, v90, 1.0
	v_rcp_f32_e32 v92, v91
	s_nop 0
	v_fma_f32 v93, -v91, v92, 1.0
	v_fmac_f32_e32 v92, v93, v92
	v_div_scale_f32 v93, vcc, 1.0, v90, 1.0
	v_mul_f32_e32 v94, v93, v92
	v_fma_f32 v95, -v91, v94, v93
	v_fmac_f32_e32 v94, v95, v92
	v_fma_f32 v91, -v91, v94, v93
	v_div_fmas_f32 v91, v91, v92, v94
	v_add_u32_e32 v92, s23, v74
	v_ashrrev_i32_e32 v93, 31, v92
	v_div_fixup_f32 v90, v91, v90, 1.0
	v_lshlrev_b64 v[92:93], 4, v[92:93]
	v_lshl_add_u64 v[94:95], s[6:7], 0, v[92:93]
	v_pk_mul_f32 v[72:73], v[72:73], v[90:91] op_sel_hi:[1,0]
	v_pk_mul_f32 v[70:71], v[70:71], v[90:91] op_sel_hi:[1,0]
	v_lshl_add_u64 v[90:91], s[10:11], 0, v[92:93]
	global_store_dwordx4 v[94:95], v[66:69], off
	global_store_dwordx4 v[90:91], v[70:73], off
	s_nop 0
	v_lshl_add_u32 v66, v66, 2, s21
	ds_add_u32 v66, v158
	v_lshl_add_u32 v66, v67, 2, s21
	ds_add_u32 v66, v158
	v_lshl_add_u32 v66, v68, 2, s21
	ds_add_u32 v66, v158
	v_lshl_add_u32 v66, v69, 2, s21
	ds_add_u32 v66, v158
	s_branch .LBB0_1513
